# speedup vs baseline: 1.0006x; 1.0006x over previous
_Z5k_fftPKtPtPKDv2_f:
	s_load_dwordx2 s[6:7], s[0:1], 0x10
	s_load_dwordx2 s[8:9], s[0:1], 0x0
	v_and_b32_e32 v1, 0xf0, v0
	v_and_b32_e32 v18, 15, v0
	v_mul_u32_u24_e32 v1, v1, v18
	v_lshlrev_b32_e32 v1, 3, v1
	s_waitcnt lgkmcnt(0)
	global_load_dwordx2 v[86:87], v1, s[6:7]
	s_lshr_b32 s4, s2, 3
	s_and_b32 s3, s2, 7
	s_and_b32 s4, s4, 0x1ffffff8
	s_or_b32 s4, s4, s3
	s_bfe_u32 s16, s2, 0x30003
	s_lshl_b32 s3, s4, 3
	s_or_b32 s3, s3, s16
	s_mov_b32 s11, 0
	s_lshr_b32 s10, s3, 1
	s_lshl_b64 s[10:11], s[10:11], 14
	s_add_u32 s3, s8, s10
	s_addc_u32 s8, s9, s11
	s_lshr_b32 s2, s2, 2
	s_and_b32 s2, s2, 2
	s_add_u32 s2, s3, s2
	v_mov_b32_e32 v3, 0
	v_lshlrev_b32_e32 v2, 2, v0
	s_addc_u32 s3, s8, 0
	s_movk_i32 s5, 0x1000
	v_lshl_add_u64 v[6:7], s[2:3], 0, v[2:3]
	v_add_co_u32_e32 v8, vcc, s5, v6
	s_movk_i32 s12, 0x2000
	s_nop 0
	v_addc_co_u32_e32 v9, vcc, 0, v7, vcc
	v_add_co_u32_e32 v10, vcc, s12, v6
	s_movk_i32 s13, 0x3000
	s_add_u32 s8, s2, 0x1000000
	v_addc_co_u32_e32 v11, vcc, 0, v7, vcc
	s_addc_u32 s9, s3, 0
	s_add_u32 s20, s2, 0x2000000
	s_addc_u32 s21, s3, 0
	v_add_co_u32_e32 v6, vcc, s13, v6
	v_lshl_add_u64 v[12:13], s[8:9], 0, v[2:3]
	s_nop 0
	v_addc_co_u32_e32 v7, vcc, 0, v7, vcc
	v_add_co_u32_e32 v14, vcc, s5, v12
	v_lshlrev_b32_e32 v1, 3, v0
	s_nop 0
	v_addc_co_u32_e32 v15, vcc, 0, v13, vcc
	v_add_co_u32_e32 v16, vcc, s12, v12
	v_or_b32_e32 v19, 0x1000, v2
	s_nop 0
	v_addc_co_u32_e32 v17, vcc, 0, v13, vcc
	v_add_co_u32_e32 v12, vcc, s13, v12
	v_or_b32_e32 v20, 0x2000, v2
	v_or_b32_e32 v21, 0x3000, v2
	v_addc_co_u32_e32 v13, vcc, 0, v13, vcc
	v_mul_u32_u24_e32 v3, 3, v0
	s_movk_i32 s5, 0x888
	v_lshlrev_b32_e32 v3, 3, v3
	s_mov_b32 s10, 0x3ec3ef15
	s_mov_b32 s11, 0xbf6c835e
	s_mov_b32 s14, s11
	s_mov_b32 s15, s10
	s_mov_b32 s12, 0xbf3504f3
	s_mov_b32 s13, s12
	v_mov_b32_e32 v88, v0
	global_load_ushort v32, v2, s[2:3] nt
	global_load_ushort v33, v2, s[8:9] nt
	global_load_ushort v34, v2, s[2:3] offset:1024 nt
	global_load_ushort v35, v2, s[8:9] offset:1024 nt
	global_load_ushort v36, v2, s[2:3] offset:2048 nt
	global_load_ushort v37, v2, s[8:9] offset:2048 nt
	global_load_ushort v38, v2, s[8:9] offset:3072 nt
	global_load_ushort v39, v2, s[2:3] offset:3072 nt
	global_load_ushort v40, v19, s[2:3] nt
	global_load_ushort v41, v19, s[8:9] nt
	global_load_ushort v42, v[8:9], off offset:1024 nt
	global_load_ushort v43, v[14:15], off offset:1024 nt
	global_load_ushort v44, v[8:9], off offset:2048 nt
	global_load_ushort v45, v[14:15], off offset:2048 nt
	global_load_ushort v46, v[14:15], off offset:3072 nt
	global_load_ushort v47, v[8:9], off offset:3072 nt
	global_load_ushort v48, v20, s[2:3] nt
	global_load_ushort v49, v20, s[8:9] nt
	global_load_ushort v50, v[10:11], off offset:1024 nt
	global_load_ushort v51, v[16:17], off offset:1024 nt
	global_load_ushort v52, v[10:11], off offset:2048 nt
	global_load_ushort v53, v[16:17], off offset:2048 nt
	global_load_ushort v54, v[16:17], off offset:3072 nt
	global_load_ushort v55, v[10:11], off offset:3072 nt
	global_load_ushort v56, v21, s[2:3] nt
	global_load_ushort v57, v21, s[8:9] nt
	global_load_ushort v58, v[6:7], off offset:1024 nt
	global_load_ushort v59, v[12:13], off offset:1024 nt
	global_load_ushort v60, v[6:7], off offset:2048 nt
	global_load_ushort v61, v[12:13], off offset:2048 nt
	global_load_ushort v62, v[12:13], off offset:3072 nt
	global_load_ushort v63, v[6:7], off offset:3072 nt
	v_mul_u32_u24_e32 v5, 5, v0
	v_mul_u32_u24_e32 v6, 6, v0
	v_mul_u32_u24_e32 v7, 7, v0
	v_mul_u32_u24_e32 v9, 9, v0
	v_mul_u32_u24_e32 v10, 10, v0
	v_lshrrev_b32_e32 v16, 1, v0
	v_lshlrev_b32_e32 v2, 4, v0
	v_lshlrev_b32_e32 v4, 5, v0
	v_lshlrev_b32_e32 v8, 6, v0
	v_mul_u32_u24_e32 v11, 11, v0
	v_mul_u32_u24_e32 v12, 12, v0
	v_mul_u32_u24_e32 v13, 13, v0
	v_mul_u32_u24_e32 v14, 14, v0
	v_mul_u32_u24_e32 v15, 15, v0
	v_lshlrev_b32_e32 v5, 3, v5
	v_lshlrev_b32_e32 v6, 3, v6
	v_lshlrev_b32_e32 v7, 3, v7
	v_lshlrev_b32_e32 v9, 3, v9
	v_lshlrev_b32_e32 v64, 3, v10
	v_and_b32_e32 v10, 0x78, v16
	v_lshlrev_b32_e32 v65, 3, v11
	v_lshlrev_b32_e32 v66, 3, v12
	v_lshlrev_b32_e32 v67, 3, v13
	v_lshlrev_b32_e32 v68, 3, v14
	v_lshlrev_b32_e32 v69, 3, v15
	v_mad_u32_u24 v96, v18, s5, v10
	global_load_dwordx2 v[30:31], v1, s[6:7]
	s_nop 0
	s_mov_b32 s6, 0x3f6c835e
	s_mov_b32 s7, 0xbec3ef15
	s_mov_b32 s8, 0x3f3504f3
	s_mov_b32 s9, s8
	s_waitcnt vmcnt(31)
	v_lshl_or_b32 v85, v33, 16, v32
	v_cvt_f32_fp8_e32 v32, v85
	s_waitcnt vmcnt(29)
	v_lshl_or_b32 v84, v35, 16, v34
	v_cvt_f32_fp8_sdwa v33, v85 src0_sel:BYTE_2
	s_waitcnt vmcnt(27)
	v_lshl_or_b32 v83, v37, 16, v36
	v_cvt_f32_fp8_e32 v34, v84
	v_cvt_f32_fp8_sdwa v35, v84 src0_sel:BYTE_2
	s_waitcnt vmcnt(25)
	v_lshl_or_b32 v82, v38, 16, v39
	s_waitcnt vmcnt(23)
	v_lshl_or_b32 v81, v41, 16, v40
	v_cvt_f32_fp8_e32 v40, v81
	s_waitcnt vmcnt(21)
	v_lshl_or_b32 v80, v43, 16, v42
	v_cvt_f32_fp8_sdwa v41, v81 src0_sel:BYTE_2
	s_waitcnt vmcnt(19)
	v_lshl_or_b32 v79, v45, 16, v44
	v_cvt_f32_fp8_e32 v42, v80
	v_cvt_f32_fp8_sdwa v43, v80 src0_sel:BYTE_2
	v_cvt_f32_fp8_e32 v36, v83
	v_cvt_f32_fp8_sdwa v37, v83 src0_sel:BYTE_2
	s_waitcnt vmcnt(17)
	v_lshl_or_b32 v78, v46, 16, v47
	v_cvt_f32_fp8_e32 v44, v79
	s_waitcnt vmcnt(15)
	v_lshl_or_b32 v77, v49, 16, v48
	v_cvt_f32_fp8_e32 v48, v77
	s_waitcnt vmcnt(13)
	v_lshl_or_b32 v76, v51, 16, v50
	v_cvt_f32_fp8_sdwa v49, v77 src0_sel:BYTE_2
	s_waitcnt vmcnt(11)
	v_lshl_or_b32 v75, v53, 16, v52
	v_cvt_f32_fp8_e32 v50, v76
	v_cvt_f32_fp8_sdwa v51, v76 src0_sel:BYTE_2
	s_waitcnt vmcnt(9)
	v_lshl_or_b32 v74, v54, 16, v55
	s_waitcnt vmcnt(7)
	v_lshl_or_b32 v73, v57, 16, v56
	v_cvt_f32_fp8_e32 v56, v73
	s_waitcnt vmcnt(5)
	v_lshl_or_b32 v72, v59, 16, v58
	v_cvt_f32_fp8_sdwa v57, v73 src0_sel:BYTE_2
	s_waitcnt vmcnt(3)
	v_lshl_or_b32 v71, v61, 16, v60
	v_cvt_f32_fp8_e32 v58, v72
	v_cvt_f32_fp8_sdwa v59, v72 src0_sel:BYTE_2
	v_cvt_f32_fp8_sdwa v45, v79 src0_sel:BYTE_2
	v_cvt_f32_fp8_e32 v52, v75
	v_cvt_f32_fp8_sdwa v53, v75 src0_sel:BYTE_2
	v_cvt_f32_fp8_e32 v60, v71
	v_cvt_f32_fp8_sdwa v61, v71 src0_sel:BYTE_2
	s_waitcnt vmcnt(1)
	v_lshl_or_b32 v70, v62, 16, v63
	v_cvt_f32_fp8_e32 v38, v82
	v_cvt_f32_fp8_sdwa v39, v82 src0_sel:BYTE_2
	v_cvt_f32_fp8_e32 v46, v78
	v_cvt_f32_fp8_sdwa v47, v78 src0_sel:BYTE_2
	v_cvt_f32_fp8_e32 v54, v74
	v_cvt_f32_fp8_sdwa v55, v74 src0_sel:BYTE_2
	v_cvt_f32_fp8_e32 v62, v70
	v_cvt_f32_fp8_sdwa v63, v70 src0_sel:BYTE_2
	v_pk_add_f32 v[64:65], v[32:33], v[48:49]
	v_pk_add_f32 v[32:33], v[32:33], v[48:49] neg_lo:[0,1] neg_hi:[0,1]
	v_pk_add_f32 v[48:49], v[40:41], v[56:57]
	v_pk_add_f32 v[40:41], v[40:41], v[56:57] neg_lo:[0,1] neg_hi:[0,1]
	v_pk_add_f32 v[56:57], v[64:65], v[48:49]
	v_pk_add_f32 v[48:49], v[64:65], v[48:49] neg_lo:[0,1] neg_hi:[0,1]
	v_pk_add_f32 v[64:65], v[32:33], v[40:41] op_sel:[0,1] op_sel_hi:[1,0] neg_hi:[0,1]
	v_pk_add_f32 v[32:33], v[32:33], v[40:41] op_sel:[0,1] op_sel_hi:[1,0] neg_lo:[0,1]
	v_pk_add_f32 v[40:41], v[34:35], v[50:51]
	v_pk_add_f32 v[34:35], v[34:35], v[50:51] neg_lo:[0,1] neg_hi:[0,1]
	v_pk_add_f32 v[50:51], v[42:43], v[58:59]
	v_pk_add_f32 v[42:43], v[42:43], v[58:59] neg_lo:[0,1] neg_hi:[0,1]
	v_pk_add_f32 v[58:59], v[40:41], v[50:51]
	v_pk_add_f32 v[40:41], v[40:41], v[50:51] neg_lo:[0,1] neg_hi:[0,1]
	v_pk_add_f32 v[50:51], v[34:35], v[42:43] op_sel:[0,1] op_sel_hi:[1,0] neg_hi:[0,1]
	v_pk_add_f32 v[34:35], v[34:35], v[42:43] op_sel:[0,1] op_sel_hi:[1,0] neg_lo:[0,1]
	v_pk_add_f32 v[42:43], v[36:37], v[52:53]
	v_pk_add_f32 v[36:37], v[36:37], v[52:53] neg_lo:[0,1] neg_hi:[0,1]
	v_pk_add_f32 v[52:53], v[44:45], v[60:61]
	v_pk_add_f32 v[44:45], v[44:45], v[60:61] neg_lo:[0,1] neg_hi:[0,1]
	v_pk_add_f32 v[60:61], v[42:43], v[52:53]
	v_pk_add_f32 v[42:43], v[42:43], v[52:53] neg_lo:[0,1] neg_hi:[0,1]
	v_pk_add_f32 v[52:53], v[36:37], v[44:45] op_sel:[0,1] op_sel_hi:[1,0] neg_hi:[0,1]
	v_pk_add_f32 v[36:37], v[36:37], v[44:45] op_sel:[0,1] op_sel_hi:[1,0] neg_lo:[0,1]
	v_pk_add_f32 v[44:45], v[38:39], v[54:55]
	v_pk_add_f32 v[38:39], v[38:39], v[54:55] neg_lo:[0,1] neg_hi:[0,1]
	v_pk_add_f32 v[54:55], v[46:47], v[62:63]
	v_pk_add_f32 v[46:47], v[46:47], v[62:63] neg_lo:[0,1] neg_hi:[0,1]
	v_pk_add_f32 v[62:63], v[44:45], v[54:55]
	v_pk_add_f32 v[44:45], v[44:45], v[54:55] neg_lo:[0,1] neg_hi:[0,1]
	v_pk_add_f32 v[54:55], v[38:39], v[46:47] op_sel:[0,1] op_sel_hi:[1,0] neg_hi:[0,1]
	v_pk_add_f32 v[38:39], v[38:39], v[46:47] op_sel:[0,1] op_sel_hi:[1,0] neg_lo:[0,1]
	v_pk_mul_f32 v[46:47], v[50:51], s[6:7] op_sel:[0,0] op_sel_hi:[0,1]
	v_pk_fma_f32 v[46:47], v[50:51], s[6:7], v[46:47] op_sel:[1,1,0] op_sel_hi:[1,0,1] neg_lo:[0,1,0]
	v_pk_mul_f32 v[50:51], v[34:35], s[10:11] op_sel:[0,0] op_sel_hi:[0,1]
	v_pk_fma_f32 v[50:51], v[34:35], s[10:11], v[50:51] op_sel:[1,1,0] op_sel_hi:[1,0,1] neg_lo:[0,1,0]
	v_pk_add_f32 v[34:35], v[52:53], v[52:53] op_sel:[0,1] op_sel_hi:[1,0] neg_hi:[0,1]
	v_pk_add_f32 v[40:41], v[40:41], v[40:41] op_sel:[0,1] op_sel_hi:[1,0] neg_hi:[0,1]
	s_nop 0
	v_pk_mul_f32 v[52:53], v[54:55], s[10:11] op_sel:[0,0] op_sel_hi:[0,1]
	v_pk_fma_f32 v[52:53], v[54:55], s[10:11], v[52:53] op_sel:[1,1,0] op_sel_hi:[1,0,1] neg_lo:[0,1,0]
	v_pk_mul_f32 v[54:55], v[38:39], s[14:15] op_sel:[0,0] op_sel_hi:[0,1]
	v_pk_fma_f32 v[54:55], v[38:39], s[14:15], v[54:55] op_sel:[1,1,0] op_sel_hi:[1,0,1] neg_lo:[0,1,0]
	v_pk_add_f32 v[38:39], v[56:57], v[60:61]
	v_pk_mul_f32 v[34:35], v[34:35], s[8:9]
	v_pk_add_f32 v[56:57], v[56:57], v[60:61] neg_lo:[0,1] neg_hi:[0,1]
	v_pk_add_f32 v[60:61], v[58:59], v[62:63]
	v_pk_add_f32 v[58:59], v[58:59], v[62:63] neg_lo:[0,1] neg_hi:[0,1]
	v_pk_mul_f32 v[40:41], v[40:41], s[8:9]
	v_pk_add_f32 v[36:37], v[36:37], v[36:37] op_sel:[0,1] op_sel_hi:[1,0] neg_lo:[0,1]
	v_pk_add_f32 v[44:45], v[44:45], v[44:45] op_sel:[0,1] op_sel_hi:[1,0] neg_lo:[0,1]
	v_pk_add_f32 v[62:63], v[38:39], v[60:61]
	v_pk_add_f32 v[38:39], v[38:39], v[60:61] neg_lo:[0,1] neg_hi:[0,1]
	v_pk_add_f32 v[60:61], v[56:57], v[58:59] op_sel:[0,1] op_sel_hi:[1,0] neg_hi:[0,1]
	v_pk_add_f32 v[56:57], v[56:57], v[58:59] op_sel:[0,1] op_sel_hi:[1,0] neg_lo:[0,1]
	v_pk_add_f32 v[58:59], v[64:65], v[34:35]
	v_pk_add_f32 v[34:35], v[64:65], v[34:35] neg_lo:[0,1] neg_hi:[0,1]
	v_pk_add_f32 v[64:65], v[46:47], v[52:53]
	v_pk_add_f32 v[46:47], v[46:47], v[52:53] neg_lo:[0,1] neg_hi:[0,1]
	v_pk_mul_f32 v[36:37], v[36:37], s[12:13]
	v_pk_mul_f32 v[44:45], v[44:45], s[12:13]
	v_pk_add_f32 v[52:53], v[58:59], v[64:65]
	v_pk_add_f32 v[58:59], v[58:59], v[64:65] neg_lo:[0,1] neg_hi:[0,1]
	v_pk_add_f32 v[64:65], v[34:35], v[46:47] op_sel:[0,1] op_sel_hi:[1,0] neg_hi:[0,1]
	v_pk_add_f32 v[34:35], v[34:35], v[46:47] op_sel:[0,1] op_sel_hi:[1,0] neg_lo:[0,1]
	v_pk_add_f32 v[46:47], v[48:49], v[42:43] op_sel:[0,1] op_sel_hi:[1,0] neg_hi:[0,1]
	v_pk_add_f32 v[42:43], v[48:49], v[42:43] op_sel:[0,1] op_sel_hi:[1,0] neg_lo:[0,1]
	v_pk_add_f32 v[48:49], v[40:41], v[44:45]
	v_pk_add_f32 v[40:41], v[40:41], v[44:45] neg_lo:[0,1] neg_hi:[0,1]
	v_pk_add_f32 v[44:45], v[48:49], v[46:47]
	v_pk_add_f32 v[46:47], v[46:47], v[48:49] neg_lo:[0,1] neg_hi:[0,1]
	v_pk_add_f32 v[48:49], v[42:43], v[40:41] op_sel:[0,1] op_sel_hi:[1,0] neg_hi:[0,1]
	v_pk_add_f32 v[40:41], v[42:43], v[40:41] op_sel:[0,1] op_sel_hi:[1,0] neg_lo:[0,1]
	v_pk_add_f32 v[42:43], v[32:33], v[36:37]
	v_pk_add_f32 v[32:33], v[32:33], v[36:37] neg_lo:[0,1] neg_hi:[0,1]
	v_pk_add_f32 v[36:37], v[50:51], v[54:55]
	v_pk_add_f32 v[50:51], v[50:51], v[54:55] neg_lo:[0,1] neg_hi:[0,1]
	v_pk_add_f32 v[54:55], v[42:43], v[36:37]
	v_pk_add_f32 v[36:37], v[42:43], v[36:37] neg_lo:[0,1] neg_hi:[0,1]
	v_pk_add_f32 v[42:43], v[32:33], v[50:51] op_sel:[0,1] op_sel_hi:[1,0] neg_hi:[0,1]
	v_pk_add_f32 v[32:33], v[32:33], v[50:51] op_sel:[0,1] op_sel_hi:[1,0] neg_lo:[0,1]
	s_waitcnt vmcnt(0)
	v_pk_mul_f32 v[28:29], v[30:31], v[30:31] op_sel:[0,0] op_sel_hi:[0,1]
	v_pk_fma_f32 v[28:29], v[30:31], v[30:31], v[28:29] op_sel:[1,1,0] op_sel_hi:[1,0,1] neg_lo:[0,1,0]
	v_pk_mul_f32 v[24:25], v[28:29], v[28:29] op_sel:[0,0] op_sel_hi:[0,1]
	v_pk_fma_f32 v[24:25], v[28:29], v[28:29], v[24:25] op_sel:[1,1,0] op_sel_hi:[1,0,1] neg_lo:[0,1,0]
	v_pk_mul_f32 v[22:23], v[24:25], v[24:25] op_sel:[0,0] op_sel_hi:[0,1]
	v_pk_fma_f32 v[22:23], v[24:25], v[24:25], v[22:23] op_sel:[1,1,0] op_sel_hi:[1,0,1] neg_lo:[0,1,0]
	v_pk_mul_f32 v[26:27], v[30:31], v[28:29] op_sel:[0,0] op_sel_hi:[0,1]
	v_pk_fma_f32 v[26:27], v[30:31], v[28:29], v[26:27] op_sel:[1,1,0] op_sel_hi:[1,0,1] neg_lo:[0,1,0]
	v_pk_mul_f32 v[20:21], v[30:31], v[24:25] op_sel:[0,0] op_sel_hi:[0,1]
	v_pk_fma_f32 v[20:21], v[30:31], v[24:25], v[20:21] op_sel:[1,1,0] op_sel_hi:[1,0,1] neg_lo:[0,1,0]
	v_pk_mul_f32 v[16:17], v[28:29], v[24:25] op_sel:[0,0] op_sel_hi:[0,1]
	v_pk_fma_f32 v[16:17], v[28:29], v[24:25], v[16:17] op_sel:[1,1,0] op_sel_hi:[1,0,1] neg_lo:[0,1,0]
	v_pk_mul_f32 v[18:19], v[30:31], v[22:23] op_sel:[0,0] op_sel_hi:[0,1]
	v_pk_fma_f32 v[18:19], v[30:31], v[22:23], v[18:19] op_sel:[1,1,0] op_sel_hi:[1,0,1] neg_lo:[0,1,0]
	v_pk_mul_f32 v[12:13], v[28:29], v[22:23] op_sel:[0,0] op_sel_hi:[0,1]
	v_pk_fma_f32 v[12:13], v[28:29], v[22:23], v[12:13] op_sel:[1,1,0] op_sel_hi:[1,0,1] neg_lo:[0,1,0]
	v_pk_mul_f32 v[6:7], v[24:25], v[22:23] op_sel:[0,0] op_sel_hi:[0,1]
	v_pk_fma_f32 v[6:7], v[24:25], v[22:23], v[6:7] op_sel:[1,1,0] op_sel_hi:[1,0,1] neg_lo:[0,1,0]
	v_pk_mul_f32 v[10:11], v[26:27], v[24:25] op_sel:[0,0] op_sel_hi:[0,1]
	v_pk_fma_f32 v[10:11], v[26:27], v[24:25], v[10:11] op_sel:[1,1,0] op_sel_hi:[1,0,1] neg_lo:[0,1,0]
	v_pk_mul_f32 v[14:15], v[26:27], v[22:23] op_sel:[0,0] op_sel_hi:[0,1]
	v_pk_fma_f32 v[14:15], v[26:27], v[22:23], v[14:15] op_sel:[1,1,0] op_sel_hi:[1,0,1] neg_lo:[0,1,0]
	v_pk_mul_f32 v[8:9], v[20:21], v[22:23] op_sel:[0,0] op_sel_hi:[0,1]
	v_pk_fma_f32 v[8:9], v[20:21], v[22:23], v[8:9] op_sel:[1,1,0] op_sel_hi:[1,0,1] neg_lo:[0,1,0]
	v_pk_mul_f32 v[4:5], v[16:17], v[22:23] op_sel:[0,0] op_sel_hi:[0,1]
	v_pk_fma_f32 v[4:5], v[16:17], v[22:23], v[4:5] op_sel:[1,1,0] op_sel_hi:[1,0,1] neg_lo:[0,1,0]
	v_pk_mul_f32 v[2:3], v[10:11], v[22:23] op_sel:[0,0] op_sel_hi:[0,1]
	v_pk_fma_f32 v[2:3], v[10:11], v[22:23], v[2:3] op_sel:[1,1,0] op_sel_hi:[1,0,1] neg_lo:[0,1,0]
	v_pk_mul_f32 v[50:51], v[52:53], v[30:31] op_sel:[0,0] op_sel_hi:[0,1]
	v_pk_fma_f32 v[50:51], v[52:53], v[30:31], v[50:51] op_sel:[1,1,0] op_sel_hi:[1,0,1] neg_lo:[0,1,0]
	ds_write_b64 v1, v[50:51] offset:2184
	v_pk_mul_f32 v[50:51], v[44:45], v[28:29] op_sel:[0,0] op_sel_hi:[0,1]
	v_pk_fma_f32 v[50:51], v[44:45], v[28:29], v[50:51] op_sel:[1,1,0] op_sel_hi:[1,0,1] neg_lo:[0,1,0]
	v_pk_mul_f32 v[44:45], v[54:55], v[26:27] op_sel:[0,0] op_sel_hi:[0,1]
	v_pk_fma_f32 v[44:45], v[54:55], v[26:27], v[44:45] op_sel:[1,1,0] op_sel_hi:[1,0,1] neg_lo:[0,1,0]
	ds_write_b64 v1, v[44:45] offset:6552
	v_pk_mul_f32 v[44:45], v[60:61], v[24:25] op_sel:[0,0] op_sel_hi:[0,1]
	v_pk_fma_f32 v[44:45], v[60:61], v[24:25], v[44:45] op_sel:[1,1,0] op_sel_hi:[1,0,1] neg_lo:[0,1,0]
	ds_write_b64 v1, v[44:45] offset:8736
	v_pk_mul_f32 v[44:45], v[64:65], v[20:21] op_sel:[0,0] op_sel_hi:[0,1]
	v_pk_fma_f32 v[44:45], v[64:65], v[20:21], v[44:45] op_sel:[1,1,0] op_sel_hi:[1,0,1] neg_lo:[0,1,0]
	ds_write_b64 v1, v[44:45] offset:10920
	v_pk_mul_f32 v[44:45], v[48:49], v[16:17] op_sel:[0,0] op_sel_hi:[0,1]
	v_pk_fma_f32 v[44:45], v[48:49], v[16:17], v[44:45] op_sel:[1,1,0] op_sel_hi:[1,0,1] neg_lo:[0,1,0]
	ds_write_b64 v1, v[44:45] offset:13104
	v_pk_mul_f32 v[44:45], v[42:43], v[10:11] op_sel:[0,0] op_sel_hi:[0,1]
	v_pk_fma_f32 v[44:45], v[42:43], v[10:11], v[44:45] op_sel:[1,1,0] op_sel_hi:[1,0,1] neg_lo:[0,1,0]
	v_pk_mul_f32 v[42:43], v[38:39], v[22:23] op_sel:[0,0] op_sel_hi:[0,1]
	v_pk_fma_f32 v[42:43], v[38:39], v[22:23], v[42:43] op_sel:[1,1,0] op_sel_hi:[1,0,1] neg_lo:[0,1,0]
	v_pk_mul_f32 v[38:39], v[58:59], v[18:19] op_sel:[0,0] op_sel_hi:[0,1]
	v_pk_fma_f32 v[38:39], v[58:59], v[18:19], v[38:39] op_sel:[1,1,0] op_sel_hi:[1,0,1] neg_lo:[0,1,0]
	ds_write_b64 v1, v[38:39] offset:19656
	v_pk_mul_f32 v[38:39], v[46:47], v[12:13] op_sel:[0,0] op_sel_hi:[0,1]
	v_pk_fma_f32 v[38:39], v[46:47], v[12:13], v[38:39] op_sel:[1,1,0] op_sel_hi:[1,0,1] neg_lo:[0,1,0]
	ds_write_b64 v1, v[38:39] offset:21840
	v_pk_mul_f32 v[38:39], v[36:37], v[14:15] op_sel:[0,0] op_sel_hi:[0,1]
	v_pk_fma_f32 v[38:39], v[36:37], v[14:15], v[38:39] op_sel:[1,1,0] op_sel_hi:[1,0,1] neg_lo:[0,1,0]
	v_pk_mul_f32 v[36:37], v[56:57], v[6:7] op_sel:[0,0] op_sel_hi:[0,1]
	v_pk_fma_f32 v[36:37], v[56:57], v[6:7], v[36:37] op_sel:[1,1,0] op_sel_hi:[1,0,1] neg_lo:[0,1,0]
	ds_write_b64 v1, v[36:37] offset:26208
	v_pk_mul_f32 v[36:37], v[34:35], v[8:9] op_sel:[0,0] op_sel_hi:[0,1]
	v_pk_fma_f32 v[36:37], v[34:35], v[8:9], v[36:37] op_sel:[1,1,0] op_sel_hi:[1,0,1] neg_lo:[0,1,0]
	v_pk_mul_f32 v[34:35], v[40:41], v[4:5] op_sel:[0,0] op_sel_hi:[0,1]
	v_pk_fma_f32 v[34:35], v[40:41], v[4:5], v[34:35] op_sel:[1,1,0] op_sel_hi:[1,0,1] neg_lo:[0,1,0]
	ds_write_b64 v1, v[34:35] offset:30576
	v_pk_mul_f32 v[34:35], v[32:33], v[2:3] op_sel:[0,0] op_sel_hi:[0,1]
	v_pk_fma_f32 v[34:35], v[32:33], v[2:3], v[34:35] op_sel:[1,1,0] op_sel_hi:[1,0,1] neg_lo:[0,1,0]
	ds_write_b64 v1, v[62:63]
	ds_write_b64 v1, v[50:51] offset:4368
	ds_write_b64 v1, v[44:45] offset:15288
	ds_write_b64 v1, v[42:43] offset:17472
	ds_write_b64 v1, v[38:39] offset:24024
	ds_write_b64 v1, v[36:37] offset:28392
	ds_write_b64 v1, v[34:35] offset:32760
	ds_write_b64 v1, v[86:87] offset:34816
	s_waitcnt lgkmcnt(0)
	s_barrier
	ds_read2_b64 v[32:35], v96 offset1:16
	ds_read2_b64 v[36:39], v96 offset0:32 offset1:48
	ds_read2_b64 v[40:43], v96 offset0:64 offset1:80
	ds_read2_b64 v[44:47], v96 offset0:128 offset1:144
	ds_read2_b64 v[48:51], v96 offset0:96 offset1:112
	ds_read2_b64 v[52:55], v96 offset0:192 offset1:208
	ds_read2_b64 v[56:59], v96 offset0:160 offset1:176
	ds_read2_b64 v[60:63], v96 offset0:224 offset1:240
	v_lshlrev_b32_e32 v115, 2, v0
	v_lshlrev_b32_e32 v119, 2, v0
	v_lshlrev_b32_e32 v123, 2, v0
	v_lshlrev_b32_e32 v127, 2, v0
	v_or_b32_e32 v119, 0x1000, v119
	v_or_b32_e32 v123, 0x2000, v123
	v_or_b32_e32 v127, 0x3000, v127
	global_load_ushort v112, v115, s[20:21]
	global_load_ushort v113, v115, s[20:21] offset:1024
	global_load_ushort v114, v115, s[20:21] offset:2048
	global_load_ushort v115, v115, s[20:21] offset:3072
	global_load_ushort v116, v119, s[20:21]
	global_load_ushort v117, v119, s[20:21] offset:1024
	global_load_ushort v118, v119, s[20:21] offset:2048
	global_load_ushort v119, v119, s[20:21] offset:3072
	global_load_ushort v120, v123, s[20:21]
	global_load_ushort v121, v123, s[20:21] offset:1024
	global_load_ushort v122, v123, s[20:21] offset:2048
	global_load_ushort v123, v123, s[20:21] offset:3072
	global_load_ushort v124, v127, s[20:21]
	global_load_ushort v125, v127, s[20:21] offset:1024
	global_load_ushort v126, v127, s[20:21] offset:2048
	global_load_ushort v127, v127, s[20:21] offset:3072
	s_waitcnt lgkmcnt(4)
	v_pk_add_f32 v[64:65], v[32:33], v[44:45]
	v_pk_add_f32 v[32:33], v[32:33], v[44:45] neg_lo:[0,1] neg_hi:[0,1]
	s_waitcnt lgkmcnt(2)
	v_pk_add_f32 v[44:45], v[40:41], v[52:53]
	v_pk_add_f32 v[40:41], v[40:41], v[52:53] neg_lo:[0,1] neg_hi:[0,1]
	v_pk_add_f32 v[52:53], v[64:65], v[44:45]
	v_pk_add_f32 v[44:45], v[64:65], v[44:45] neg_lo:[0,1] neg_hi:[0,1]
	v_pk_add_f32 v[64:65], v[32:33], v[40:41] op_sel:[0,1] op_sel_hi:[1,0] neg_hi:[0,1]
	v_pk_add_f32 v[32:33], v[32:33], v[40:41] op_sel:[0,1] op_sel_hi:[1,0] neg_lo:[0,1]
	v_pk_add_f32 v[40:41], v[34:35], v[46:47]
	v_pk_add_f32 v[34:35], v[34:35], v[46:47] neg_lo:[0,1] neg_hi:[0,1]
	v_pk_add_f32 v[46:47], v[42:43], v[54:55]
	v_pk_add_f32 v[42:43], v[42:43], v[54:55] neg_lo:[0,1] neg_hi:[0,1]
	v_pk_add_f32 v[54:55], v[40:41], v[46:47]
	v_pk_add_f32 v[40:41], v[40:41], v[46:47] neg_lo:[0,1] neg_hi:[0,1]
	v_pk_add_f32 v[46:47], v[34:35], v[42:43] op_sel:[0,1] op_sel_hi:[1,0] neg_hi:[0,1]
	v_pk_add_f32 v[34:35], v[34:35], v[42:43] op_sel:[0,1] op_sel_hi:[1,0] neg_lo:[0,1]
	s_waitcnt lgkmcnt(1)
	v_pk_add_f32 v[42:43], v[36:37], v[56:57]
	v_pk_add_f32 v[36:37], v[36:37], v[56:57] neg_lo:[0,1] neg_hi:[0,1]
	s_waitcnt lgkmcnt(0)
	v_pk_add_f32 v[56:57], v[48:49], v[60:61]
	v_pk_add_f32 v[48:49], v[48:49], v[60:61] neg_lo:[0,1] neg_hi:[0,1]
	v_pk_add_f32 v[60:61], v[42:43], v[56:57]
	v_pk_add_f32 v[42:43], v[42:43], v[56:57] neg_lo:[0,1] neg_hi:[0,1]
	v_pk_add_f32 v[56:57], v[36:37], v[48:49] op_sel:[0,1] op_sel_hi:[1,0] neg_hi:[0,1]
	v_pk_add_f32 v[36:37], v[36:37], v[48:49] op_sel:[0,1] op_sel_hi:[1,0] neg_lo:[0,1]
	v_pk_add_f32 v[48:49], v[38:39], v[58:59]
	v_pk_add_f32 v[38:39], v[38:39], v[58:59] neg_lo:[0,1] neg_hi:[0,1]
	v_pk_add_f32 v[58:59], v[50:51], v[62:63]
	v_pk_add_f32 v[50:51], v[50:51], v[62:63] neg_lo:[0,1] neg_hi:[0,1]
	v_pk_add_f32 v[62:63], v[48:49], v[58:59]
	v_pk_add_f32 v[48:49], v[48:49], v[58:59] neg_lo:[0,1] neg_hi:[0,1]
	v_pk_add_f32 v[58:59], v[38:39], v[50:51] op_sel:[0,1] op_sel_hi:[1,0] neg_hi:[0,1]
	v_pk_add_f32 v[38:39], v[38:39], v[50:51] op_sel:[0,1] op_sel_hi:[1,0] neg_lo:[0,1]
	v_pk_mul_f32 v[50:51], v[46:47], s[6:7] op_sel:[0,0] op_sel_hi:[0,1]
	v_pk_fma_f32 v[50:51], v[46:47], s[6:7], v[50:51] op_sel:[1,1,0] op_sel_hi:[1,0,1] neg_lo:[0,1,0]
	v_pk_mul_f32 v[46:47], v[34:35], s[10:11] op_sel:[0,0] op_sel_hi:[0,1]
	v_pk_fma_f32 v[46:47], v[34:35], s[10:11], v[46:47] op_sel:[1,1,0] op_sel_hi:[1,0,1] neg_lo:[0,1,0]
	v_pk_add_f32 v[34:35], v[56:57], v[56:57] op_sel:[0,1] op_sel_hi:[1,0] neg_hi:[0,1]
	v_pk_add_f32 v[40:41], v[40:41], v[40:41] op_sel:[0,1] op_sel_hi:[1,0] neg_hi:[0,1]
	s_nop 0
	v_pk_mul_f32 v[56:57], v[58:59], s[10:11] op_sel:[0,0] op_sel_hi:[0,1]
	v_pk_fma_f32 v[56:57], v[58:59], s[10:11], v[56:57] op_sel:[1,1,0] op_sel_hi:[1,0,1] neg_lo:[0,1,0]
	v_pk_mul_f32 v[58:59], v[38:39], s[14:15] op_sel:[0,0] op_sel_hi:[0,1]
	v_pk_fma_f32 v[58:59], v[38:39], s[14:15], v[58:59] op_sel:[1,1,0] op_sel_hi:[1,0,1] neg_lo:[0,1,0]
	v_pk_add_f32 v[38:39], v[52:53], v[60:61]
	v_pk_mul_f32 v[34:35], v[34:35], s[8:9]
	v_pk_add_f32 v[52:53], v[52:53], v[60:61] neg_lo:[0,1] neg_hi:[0,1]
	v_pk_add_f32 v[60:61], v[54:55], v[62:63]
	v_pk_add_f32 v[54:55], v[54:55], v[62:63] neg_lo:[0,1] neg_hi:[0,1]
	v_pk_add_f32 v[36:37], v[36:37], v[36:37] op_sel:[0,1] op_sel_hi:[1,0] neg_lo:[0,1]
	v_pk_add_f32 v[48:49], v[48:49], v[48:49] op_sel:[0,1] op_sel_hi:[1,0] neg_lo:[0,1]
	v_pk_add_f32 v[62:63], v[38:39], v[60:61]
	v_pk_add_f32 v[60:61], v[38:39], v[60:61] neg_lo:[0,1] neg_hi:[0,1]
	v_pk_add_f32 v[66:67], v[52:53], v[54:55] op_sel:[0,1] op_sel_hi:[1,0] neg_hi:[0,1]
	v_pk_add_f32 v[52:53], v[52:53], v[54:55] op_sel:[0,1] op_sel_hi:[1,0] neg_lo:[0,1]
	v_pk_add_f32 v[38:39], v[64:65], v[34:35]
	v_pk_add_f32 v[34:35], v[64:65], v[34:35] neg_lo:[0,1] neg_hi:[0,1]
	v_pk_add_f32 v[54:55], v[50:51], v[56:57]
	v_pk_add_f32 v[50:51], v[50:51], v[56:57] neg_lo:[0,1] neg_hi:[0,1]
	v_pk_mul_f32 v[40:41], v[40:41], s[8:9]
	v_pk_mul_f32 v[36:37], v[36:37], s[12:13]
	v_pk_mul_f32 v[48:49], v[48:49], s[12:13]
	v_pk_add_f32 v[56:57], v[38:39], v[54:55]
	v_pk_add_f32 v[54:55], v[38:39], v[54:55] neg_lo:[0,1] neg_hi:[0,1]
	v_pk_add_f32 v[64:65], v[34:35], v[50:51] op_sel:[0,1] op_sel_hi:[1,0] neg_hi:[0,1]
	v_pk_add_f32 v[50:51], v[34:35], v[50:51] op_sel:[0,1] op_sel_hi:[1,0] neg_lo:[0,1]
	v_pk_add_f32 v[34:35], v[44:45], v[42:43] op_sel:[0,1] op_sel_hi:[1,0] neg_hi:[0,1]
	v_pk_add_f32 v[38:39], v[44:45], v[42:43] op_sel:[0,1] op_sel_hi:[1,0] neg_lo:[0,1]
	v_pk_add_f32 v[42:43], v[40:41], v[48:49]
	v_pk_add_f32 v[40:41], v[40:41], v[48:49] neg_lo:[0,1] neg_hi:[0,1]
	v_pk_add_f32 v[44:45], v[42:43], v[34:35]
	v_pk_add_f32 v[42:43], v[34:35], v[42:43] neg_lo:[0,1] neg_hi:[0,1]
	v_pk_add_f32 v[34:35], v[32:33], v[36:37]
	v_pk_add_f32 v[36:37], v[32:33], v[36:37] neg_lo:[0,1] neg_hi:[0,1]
	v_pk_add_f32 v[32:33], v[46:47], v[58:59]
	v_pk_add_f32 v[48:49], v[38:39], v[40:41] op_sel:[0,1] op_sel_hi:[1,0] neg_hi:[0,1]
	v_pk_add_f32 v[40:41], v[38:39], v[40:41] op_sel:[0,1] op_sel_hi:[1,0] neg_lo:[0,1]
	v_pk_add_f32 v[38:39], v[46:47], v[58:59] neg_lo:[0,1] neg_hi:[0,1]
	v_pk_add_f32 v[46:47], v[34:35], v[32:33]
	v_pk_add_f32 v[58:59], v[34:35], v[32:33] neg_lo:[0,1] neg_hi:[0,1]
	v_pk_add_f32 v[68:69], v[36:37], v[38:39] op_sel:[0,1] op_sel_hi:[1,0] neg_hi:[0,1]
	v_pk_add_f32 v[86:87], v[36:37], v[38:39] op_sel:[0,1] op_sel_hi:[1,0] neg_lo:[0,1]
	s_nop 0
	v_ashrrev_i32_e32 v32, 4, v88
	v_lshlrev_b32_e32 v90, 3, v32
	v_add_u32_e32 v91, 0x8800, v90
	v_and_b32_e32 v36, 15, v88
	ds_read2_b64 v[32:35], v91 offset0:16 offset1:32
	v_mad_u32_u24 v92, v36, s5, v90
	ds_read2_b64 v[36:39], v91 offset0:48 offset1:64
	s_waitcnt lgkmcnt(1)
	v_pk_mul_f32 v[88:89], v[56:57], v[32:33] op_sel:[0,0] op_sel_hi:[0,1]
	v_pk_fma_f32 v[88:89], v[56:57], v[32:33], v[88:89] op_sel:[1,1,0] op_sel_hi:[1,0,1] neg_lo:[0,1,0]
	v_pk_mul_f32 v[56:57], v[44:45], v[34:35] op_sel:[0,0] op_sel_hi:[0,1]
	v_pk_fma_f32 v[56:57], v[44:45], v[34:35], v[56:57] op_sel:[1,1,0] op_sel_hi:[1,0,1] neg_lo:[0,1,0]
	s_waitcnt lgkmcnt(0)
	v_pk_mul_f32 v[44:45], v[46:47], v[36:37] op_sel:[0,0] op_sel_hi:[0,1]
	v_pk_fma_f32 v[44:45], v[46:47], v[36:37], v[44:45] op_sel:[1,1,0] op_sel_hi:[1,0,1] neg_lo:[0,1,0]
	ds_write2_b64 v92, v[56:57], v[44:45] offset0:32 offset1:48
	v_pk_mul_f32 v[44:45], v[66:67], v[38:39] op_sel:[0,0] op_sel_hi:[0,1]
	v_pk_fma_f32 v[44:45], v[66:67], v[38:39], v[44:45] op_sel:[1,1,0] op_sel_hi:[1,0,1] neg_lo:[0,1,0]
	ds_read2_b64 v[32:35], v91 offset0:80 offset1:96
	s_waitcnt lgkmcnt(0)
	v_pk_mul_f32 v[46:47], v[64:65], v[32:33] op_sel:[0,0] op_sel_hi:[0,1]
	v_pk_fma_f32 v[46:47], v[64:65], v[32:33], v[46:47] op_sel:[1,1,0] op_sel_hi:[1,0,1] neg_lo:[0,1,0]
	ds_write2_b64 v92, v[44:45], v[46:47] offset0:64 offset1:80
	v_pk_mul_f32 v[44:45], v[48:49], v[34:35] op_sel:[0,0] op_sel_hi:[0,1]
	v_pk_fma_f32 v[44:45], v[48:49], v[34:35], v[44:45] op_sel:[1,1,0] op_sel_hi:[1,0,1] neg_lo:[0,1,0]
	ds_read2_b64 v[36:39], v91 offset0:112 offset1:128
	ds_read2_b64 v[32:35], v91 offset0:144 offset1:160
	s_waitcnt lgkmcnt(1)
	v_pk_mul_f32 v[46:47], v[68:69], v[36:37] op_sel:[0,0] op_sel_hi:[0,1]
	v_pk_fma_f32 v[46:47], v[68:69], v[36:37], v[46:47] op_sel:[1,1,0] op_sel_hi:[1,0,1] neg_lo:[0,1,0]
	ds_write2_b64 v92, v[44:45], v[46:47] offset0:96 offset1:112
	v_pk_mul_f32 v[44:45], v[60:61], v[38:39] op_sel:[0,0] op_sel_hi:[0,1]
	v_pk_fma_f32 v[44:45], v[60:61], v[38:39], v[44:45] op_sel:[1,1,0] op_sel_hi:[1,0,1] neg_lo:[0,1,0]
	ds_read2_b64 v[36:39], v91 offset0:176 offset1:192
	s_waitcnt lgkmcnt(2)
	v_pk_mul_f32 v[46:47], v[54:55], v[32:33] op_sel:[0,0] op_sel_hi:[0,1]
	v_pk_fma_f32 v[46:47], v[54:55], v[32:33], v[46:47] op_sel:[1,1,0] op_sel_hi:[1,0,1] neg_lo:[0,1,0]
	ds_write2_b64 v92, v[44:45], v[46:47] offset0:128 offset1:144
	v_pk_mul_f32 v[44:45], v[42:43], v[34:35] op_sel:[0,0] op_sel_hi:[0,1]
	v_pk_fma_f32 v[44:45], v[42:43], v[34:35], v[44:45] op_sel:[1,1,0] op_sel_hi:[1,0,1] neg_lo:[0,1,0]
	ds_read2_b64 v[32:35], v91 offset0:208 offset1:224
	s_waitcnt lgkmcnt(2)
	v_pk_mul_f32 v[42:43], v[58:59], v[36:37] op_sel:[0,0] op_sel_hi:[0,1]
	v_pk_fma_f32 v[42:43], v[58:59], v[36:37], v[42:43] op_sel:[1,1,0] op_sel_hi:[1,0,1] neg_lo:[0,1,0]
	ds_write2_b64 v92, v[44:45], v[42:43] offset0:160 offset1:176
	v_pk_mul_f32 v[42:43], v[52:53], v[38:39] op_sel:[0,0] op_sel_hi:[0,1]
	v_pk_fma_f32 v[42:43], v[52:53], v[38:39], v[42:43] op_sel:[1,1,0] op_sel_hi:[1,0,1] neg_lo:[0,1,0]
	s_waitcnt lgkmcnt(1)
	v_pk_mul_f32 v[38:39], v[50:51], v[32:33] op_sel:[0,0] op_sel_hi:[0,1]
	v_pk_fma_f32 v[38:39], v[50:51], v[32:33], v[38:39] op_sel:[1,1,0] op_sel_hi:[1,0,1] neg_lo:[0,1,0]
	v_pk_mul_f32 v[32:33], v[40:41], v[34:35] op_sel:[0,0] op_sel_hi:[0,1]
	v_pk_fma_f32 v[32:33], v[40:41], v[34:35], v[32:33] op_sel:[1,1,0] op_sel_hi:[1,0,1] neg_lo:[0,1,0]
	ds_read_b64 v[36:37], v90 offset:36736
	s_waitcnt lgkmcnt(0)
	v_pk_mul_f32 v[34:35], v[86:87], v[36:37] op_sel:[0,0] op_sel_hi:[0,1]
	v_pk_fma_f32 v[34:35], v[86:87], v[36:37], v[34:35] op_sel:[1,1,0] op_sel_hi:[1,0,1] neg_lo:[0,1,0]
	ds_write2_b64 v92, v[32:33], v[34:35] offset0:224 offset1:240
	v_mov_b32_e32 v32, v0
	ds_write2_b64 v92, v[62:63], v[88:89] offset1:16
	ds_write2_b64 v92, v[42:43], v[38:39] offset0:192 offset1:208
	s_waitcnt lgkmcnt(0)
	s_barrier
	s_nop 0
	v_and_b32_e32 v33, 15, v32
	v_and_b32_e32 v32, 0x1ffffff0, v32
	v_lshlrev_b32_e32 v32, 3, v32
	v_mad_u32_u24 v60, v33, s5, v32
	ds_read2_b64 v[32:35], v60 offset1:1
	ds_read2_b64 v[36:39], v60 offset0:2 offset1:3
	ds_read2_b64 v[40:43], v60 offset0:8 offset1:9
	ds_read2_b64 v[44:47], v60 offset0:4 offset1:5
	ds_read2_b64 v[48:51], v60 offset0:6 offset1:7
	ds_read2_b64 v[52:55], v60 offset0:12 offset1:13
	ds_read2_b64 v[56:59], v60 offset0:10 offset1:11
	ds_read2_b64 v[60:63], v60 offset0:14 offset1:15
	s_waitcnt lgkmcnt(5)
	v_pk_add_f32 v[64:65], v[32:33], v[40:41]
	v_pk_add_f32 v[32:33], v[32:33], v[40:41] neg_lo:[0,1] neg_hi:[0,1]
	s_waitcnt lgkmcnt(2)
	v_pk_add_f32 v[40:41], v[44:45], v[52:53]
	v_pk_add_f32 v[44:45], v[44:45], v[52:53] neg_lo:[0,1] neg_hi:[0,1]
	v_pk_add_f32 v[52:53], v[64:65], v[40:41]
	v_pk_add_f32 v[40:41], v[64:65], v[40:41] neg_lo:[0,1] neg_hi:[0,1]
	v_pk_add_f32 v[64:65], v[32:33], v[44:45] op_sel:[0,1] op_sel_hi:[1,0] neg_hi:[0,1]
	v_pk_add_f32 v[66:67], v[32:33], v[44:45] op_sel:[0,1] op_sel_hi:[1,0] neg_lo:[0,1]
	v_pk_add_f32 v[32:33], v[34:35], v[42:43]
	v_pk_add_f32 v[34:35], v[34:35], v[42:43] neg_lo:[0,1] neg_hi:[0,1]
	v_pk_add_f32 v[42:43], v[46:47], v[54:55]
	v_pk_add_f32 v[44:45], v[46:47], v[54:55] neg_lo:[0,1] neg_hi:[0,1]
	v_pk_add_f32 v[46:47], v[32:33], v[42:43]
	v_pk_add_f32 v[32:33], v[32:33], v[42:43] neg_lo:[0,1] neg_hi:[0,1]
	v_pk_add_f32 v[42:43], v[34:35], v[44:45] op_sel:[0,1] op_sel_hi:[1,0] neg_hi:[0,1]
	v_pk_add_f32 v[34:35], v[34:35], v[44:45] op_sel:[0,1] op_sel_hi:[1,0] neg_lo:[0,1]
	s_waitcnt lgkmcnt(1)
	v_pk_add_f32 v[44:45], v[36:37], v[56:57]
	s_waitcnt lgkmcnt(0)
	v_pk_add_f32 v[54:55], v[48:49], v[60:61]
	v_pk_add_f32 v[32:33], v[32:33], v[32:33] op_sel:[0,1] op_sel_hi:[1,0] neg_hi:[0,1]
	v_pk_add_f32 v[36:37], v[36:37], v[56:57] neg_lo:[0,1] neg_hi:[0,1]
	v_pk_add_f32 v[48:49], v[48:49], v[60:61] neg_lo:[0,1] neg_hi:[0,1]
	v_pk_add_f32 v[56:57], v[44:45], v[54:55]
	v_pk_add_f32 v[54:55], v[44:45], v[54:55] neg_lo:[0,1] neg_hi:[0,1]
	v_pk_add_f32 v[44:45], v[36:37], v[48:49] op_sel:[0,1] op_sel_hi:[1,0] neg_hi:[0,1]
	v_pk_mul_f32 v[68:69], v[32:33], s[8:9]
	v_pk_add_f32 v[36:37], v[36:37], v[48:49] op_sel:[0,1] op_sel_hi:[1,0] neg_lo:[0,1]
	v_pk_add_f32 v[48:49], v[38:39], v[58:59]
	v_pk_add_f32 v[32:33], v[44:45], v[44:45] op_sel:[0,1] op_sel_hi:[1,0] neg_hi:[0,1]
	v_pk_add_f32 v[38:39], v[38:39], v[58:59] neg_lo:[0,1] neg_hi:[0,1]
	v_pk_add_f32 v[58:59], v[50:51], v[62:63]
	v_pk_mul_f32 v[86:87], v[34:35], s[10:11] op_sel:[0,0] op_sel_hi:[0,1]
	v_pk_fma_f32 v[86:87], v[34:35], s[10:11], v[86:87] op_sel:[1,1,0] op_sel_hi:[1,0,1] neg_lo:[0,1,0]
	v_pk_mul_f32 v[34:35], v[32:33], s[8:9]
	v_pk_add_f32 v[32:33], v[36:37], v[36:37] op_sel:[0,1] op_sel_hi:[1,0] neg_lo:[0,1]
	v_pk_add_f32 v[50:51], v[50:51], v[62:63] neg_lo:[0,1] neg_hi:[0,1]
	v_pk_add_f32 v[60:61], v[48:49], v[58:59]
	v_pk_add_f32 v[48:49], v[48:49], v[58:59] neg_lo:[0,1] neg_hi:[0,1]
	v_pk_add_f32 v[58:59], v[38:39], v[50:51] op_sel:[0,1] op_sel_hi:[1,0] neg_hi:[0,1]
	v_pk_add_f32 v[38:39], v[38:39], v[50:51] op_sel:[0,1] op_sel_hi:[1,0] neg_lo:[0,1]
	v_pk_mul_f32 v[88:89], v[32:33], s[12:13]
	v_pk_add_f32 v[36:37], v[46:47], v[60:61]
	v_pk_add_f32 v[32:33], v[48:49], v[48:49] op_sel:[0,1] op_sel_hi:[1,0] neg_lo:[0,1]
	v_pk_mul_f32 v[44:45], v[58:59], s[10:11] op_sel:[0,0] op_sel_hi:[0,1]
	v_pk_fma_f32 v[44:45], v[58:59], s[10:11], v[44:45] op_sel:[1,1,0] op_sel_hi:[1,0,1] neg_lo:[0,1,0]
	v_pk_mul_f32 v[58:59], v[38:39], s[14:15] op_sel:[0,0] op_sel_hi:[0,1]
	v_pk_fma_f32 v[58:59], v[38:39], s[14:15], v[58:59] op_sel:[1,1,0] op_sel_hi:[1,0,1] neg_lo:[0,1,0]
	v_pk_add_f32 v[38:39], v[52:53], v[56:57] neg_lo:[0,1] neg_hi:[0,1]
	v_pk_mul_f32 v[48:49], v[32:33], s[12:13]
	v_pk_add_f32 v[32:33], v[52:53], v[56:57]
	v_pk_add_f32 v[46:47], v[46:47], v[60:61] neg_lo:[0,1] neg_hi:[0,1]
	v_pk_mul_f32 v[62:63], v[42:43], s[6:7] op_sel:[0,0] op_sel_hi:[0,1]
	v_pk_fma_f32 v[62:63], v[42:43], s[6:7], v[62:63] op_sel:[1,1,0] op_sel_hi:[1,0,1] neg_lo:[0,1,0]
	v_pk_add_f32 v[50:51], v[32:33], v[36:37]
	v_pk_add_f32 v[36:37], v[32:33], v[36:37] neg_lo:[0,1] neg_hi:[0,1]
	v_pk_add_f32 v[42:43], v[38:39], v[46:47] op_sel:[0,1] op_sel_hi:[1,0] neg_hi:[0,1]
	v_pk_add_f32 v[32:33], v[38:39], v[46:47] op_sel:[0,1] op_sel_hi:[1,0] neg_lo:[0,1]
	v_pk_add_f32 v[38:39], v[64:65], v[34:35]
	v_pk_add_f32 v[34:35], v[64:65], v[34:35] neg_lo:[0,1] neg_hi:[0,1]
	v_pk_add_f32 v[46:47], v[62:63], v[44:45]
	v_pk_add_f32 v[56:57], v[62:63], v[44:45] neg_lo:[0,1] neg_hi:[0,1]
	v_pk_add_f32 v[52:53], v[38:39], v[46:47]
	v_pk_add_f32 v[38:39], v[38:39], v[46:47] neg_lo:[0,1] neg_hi:[0,1]
	v_pk_add_f32 v[44:45], v[34:35], v[56:57] op_sel:[0,1] op_sel_hi:[1,0] neg_hi:[0,1]
	v_pk_add_f32 v[34:35], v[34:35], v[56:57] op_sel:[0,1] op_sel_hi:[1,0] neg_lo:[0,1]
	v_pk_add_f32 v[46:47], v[40:41], v[54:55] op_sel:[0,1] op_sel_hi:[1,0] neg_hi:[0,1]
	v_pk_add_f32 v[56:57], v[40:41], v[54:55] op_sel:[0,1] op_sel_hi:[1,0] neg_lo:[0,1]
	v_pk_add_f32 v[40:41], v[68:69], v[48:49]
	v_pk_add_f32 v[60:61], v[68:69], v[48:49] neg_lo:[0,1] neg_hi:[0,1]
	v_pk_add_f32 v[54:55], v[40:41], v[46:47]
	v_pk_add_f32 v[40:41], v[46:47], v[40:41] neg_lo:[0,1] neg_hi:[0,1]
	v_pk_add_f32 v[46:47], v[66:67], v[88:89]
	v_pk_add_f32 v[62:63], v[86:87], v[58:59]
	v_pk_add_f32 v[58:59], v[86:87], v[58:59] neg_lo:[0,1] neg_hi:[0,1]
	v_pk_add_f32 v[48:49], v[56:57], v[60:61] op_sel:[0,1] op_sel_hi:[1,0] neg_hi:[0,1]
	v_pk_add_f32 v[64:65], v[56:57], v[60:61] op_sel:[0,1] op_sel_hi:[1,0] neg_lo:[0,1]
	v_pk_add_f32 v[60:61], v[66:67], v[88:89] neg_lo:[0,1] neg_hi:[0,1]
	v_pk_add_f32 v[56:57], v[46:47], v[62:63]
	v_pk_add_f32 v[68:69], v[46:47], v[62:63] neg_lo:[0,1] neg_hi:[0,1]
	v_pk_add_f32 v[46:47], v[60:61], v[58:59] op_sel:[0,1] op_sel_hi:[1,0] neg_hi:[0,1]
	v_pk_add_f32 v[66:67], v[60:61], v[58:59] op_sel:[0,1] op_sel_hi:[1,0] neg_lo:[0,1]
	v_mov_b32_e32 v58, v0
	s_nop 0
	v_and_b32_e32 v59, -16, v58
	v_and_b32_e32 v60, 15, v58
	v_lshlrev_b32_e32 v61, 3, v59
	v_mad_u32_u24 v61, v60, s5, v61
	v_cmp_ne_u32_e32 vcc, 0, v60
	ds_write2_b64 v61, v[50:51], v[52:53] offset1:1
	ds_write2_b64 v61, v[54:55], v[56:57] offset0:2 offset1:3
	ds_write2_b64 v61, v[42:43], v[44:45] offset0:4 offset1:5
	ds_write2_b64 v61, v[48:49], v[46:47] offset0:6 offset1:7
	ds_write2_b64 v61, v[36:37], v[38:39] offset0:8 offset1:9
	ds_write2_b64 v61, v[40:41], v[68:69] offset0:10 offset1:11
	ds_write2_b64 v61, v[32:33], v[34:35] offset0:12 offset1:13
	ds_write2_b64 v61, v[64:65], v[66:67] offset0:14 offset1:15
	s_waitcnt lgkmcnt(0)
	s_barrier
	s_and_saveexec_b64 s[6:7], vcc
	s_xor_b64 s[6:7], exec, s[6:7]
	v_sub_u32_e32 v60, 16, v60
	v_mul_u32_u24_e32 v60, 0x111, v60
	v_sub_u32_e32 v59, v60, v59
	v_add_u32_e32 v61, 0xf0, v59
	s_andn2_saveexec_b64 s[6:7], s[6:7]
	v_sub_u32_e32 v59, 0x100, v58
	v_cmp_lt_u32_e32 vcc, 15, v58
	s_nop 1
	v_cndmask_b32_e32 v61, 1, v59, vcc
	s_or_b64 exec, exec, s[6:7]
	v_mov_b32_e32 v59, 0
	v_lshlrev_b32_e32 v92, 3, v61
	ds_read_b64 v[90:91], v59
	ds_read2_b64 v[60:63], v92 offset0:14 offset1:15
	ds_read2_b64 v[86:89], v92 offset0:12 offset1:13
	v_cmp_eq_u32_e32 vcc, 0, v58
	v_cvt_f32_fp8_sdwa v93, v74 src0_sel:BYTE_3
	v_cvt_f32_fp8_sdwa v94, v72 src0_sel:BYTE_1
	s_waitcnt lgkmcnt(1)
	v_cndmask_b32_e32 v59, v63, v91, vcc
	v_cndmask_b32_e32 v58, v62, v90, vcc
	v_pk_add_f32 v[90:91], v[50:51], v[58:59] neg_hi:[0,1]
	v_pk_add_f32 v[50:51], v[50:51], v[58:59] neg_lo:[0,1]
	v_cvt_f32_fp8_sdwa v95, v72 src0_sel:BYTE_3
	v_pk_mul_f32 v[62:63], v[90:91], v[50:51] op_sel:[0,0] op_sel_hi:[0,1]
	v_pk_fma_f32 v[62:63], v[90:91], v[50:51], v[62:63] op_sel:[1,1,0] op_sel_hi:[1,0,1] neg_hi:[0,1,0]
	v_pk_add_f32 v[50:51], v[52:53], v[60:61] neg_hi:[0,1]
	v_pk_add_f32 v[52:53], v[52:53], v[60:61] neg_lo:[0,1]
	v_cvt_f32_fp8_sdwa v72, v71 src0_sel:BYTE_1
	v_pk_mul_f32 v[60:61], v[50:51], v[52:53] op_sel:[0,0] op_sel_hi:[0,1]
	v_pk_fma_f32 v[60:61], v[50:51], v[52:53], v[60:61] op_sel:[1,1,0] op_sel_hi:[1,0,1] neg_hi:[0,1,0]
	s_waitcnt lgkmcnt(0)
	v_pk_add_f32 v[50:51], v[54:55], v[88:89] neg_hi:[0,1]
	v_pk_add_f32 v[52:53], v[54:55], v[88:89] neg_lo:[0,1]
	v_pk_add_f32 v[54:55], v[56:57], v[86:87] neg_hi:[0,1]
	v_pk_add_f32 v[86:87], v[56:57], v[86:87] neg_lo:[0,1]
	v_cvt_f32_fp8_sdwa v98, v70 src0_sel:BYTE_1
	v_pk_mul_f32 v[58:59], v[50:51], v[52:53] op_sel:[0,0] op_sel_hi:[0,1]
	v_pk_fma_f32 v[58:59], v[50:51], v[52:53], v[58:59] op_sel:[1,1,0] op_sel_hi:[1,0,1] neg_hi:[0,1,0]
	ds_read2_b64 v[50:53], v92 offset0:10 offset1:11
	v_pk_mul_f32 v[56:57], v[54:55], v[86:87] op_sel:[0,0] op_sel_hi:[0,1]
	v_pk_fma_f32 v[56:57], v[54:55], v[86:87], v[56:57] op_sel:[1,1,0] op_sel_hi:[1,0,1] neg_hi:[0,1,0]
	ds_read2_b64 v[86:89], v92 offset0:8 offset1:9
	s_waitcnt lgkmcnt(1)
	v_pk_add_f32 v[90:91], v[42:43], v[52:53] neg_hi:[0,1]
	v_pk_add_f32 v[42:43], v[42:43], v[52:53] neg_lo:[0,1]
	v_cvt_f32_fp8_sdwa v99, v70 src0_sel:BYTE_3
	v_pk_mul_f32 v[54:55], v[90:91], v[42:43] op_sel:[0,0] op_sel_hi:[0,1]
	v_pk_fma_f32 v[54:55], v[90:91], v[42:43], v[54:55] op_sel:[1,1,0] op_sel_hi:[1,0,1] neg_hi:[0,1,0]
	v_pk_add_f32 v[42:43], v[44:45], v[50:51] neg_hi:[0,1]
	v_pk_add_f32 v[44:45], v[44:45], v[50:51] neg_lo:[0,1]
	s_mov_b32 s6, 0x3f6c835e
	v_pk_mul_f32 v[52:53], v[42:43], v[44:45] op_sel:[0,0] op_sel_hi:[0,1]
	v_pk_fma_f32 v[52:53], v[42:43], v[44:45], v[52:53] op_sel:[1,1,0] op_sel_hi:[1,0,1] neg_hi:[0,1,0]
	s_waitcnt lgkmcnt(0)
	v_pk_add_f32 v[42:43], v[48:49], v[88:89] neg_hi:[0,1]
	v_pk_add_f32 v[44:45], v[48:49], v[88:89] neg_lo:[0,1]
	v_pk_add_f32 v[88:89], v[46:47], v[86:87] neg_hi:[0,1]
	v_pk_add_f32 v[46:47], v[46:47], v[86:87] neg_lo:[0,1]
	s_mov_b32 s7, 0xbec3ef15
	v_pk_mul_f32 v[50:51], v[42:43], v[44:45] op_sel:[0,0] op_sel_hi:[0,1]
	v_pk_fma_f32 v[50:51], v[42:43], v[44:45], v[50:51] op_sel:[1,1,0] op_sel_hi:[1,0,1] neg_hi:[0,1,0]
	ds_read2_b64 v[42:45], v92 offset0:6 offset1:7
	v_pk_mul_f32 v[48:49], v[88:89], v[46:47] op_sel:[0,0] op_sel_hi:[0,1]
	v_pk_fma_f32 v[48:49], v[88:89], v[46:47], v[48:49] op_sel:[1,1,0] op_sel_hi:[1,0,1] neg_hi:[0,1,0]
	ds_read2_b64 v[86:89], v92 offset0:4 offset1:5
	s_waitcnt lgkmcnt(1)
	v_pk_add_f32 v[90:91], v[36:37], v[44:45] neg_hi:[0,1]
	v_pk_add_f32 v[36:37], v[36:37], v[44:45] neg_lo:[0,1]
	s_mov_b32 s9, s8
	v_pk_mul_f32 v[46:47], v[90:91], v[36:37] op_sel:[0,0] op_sel_hi:[0,1]
	v_pk_fma_f32 v[46:47], v[90:91], v[36:37], v[46:47] op_sel:[1,1,0] op_sel_hi:[1,0,1] neg_hi:[0,1,0]
	v_pk_add_f32 v[36:37], v[38:39], v[42:43] neg_hi:[0,1]
	v_pk_add_f32 v[38:39], v[38:39], v[42:43] neg_lo:[0,1]
	v_cvt_f32_fp8_sdwa v90, v76 src0_sel:BYTE_1
	v_pk_mul_f32 v[44:45], v[36:37], v[38:39] op_sel:[0,0] op_sel_hi:[0,1]
	v_pk_fma_f32 v[44:45], v[36:37], v[38:39], v[44:45] op_sel:[1,1,0] op_sel_hi:[1,0,1] neg_hi:[0,1,0]
	s_waitcnt lgkmcnt(0)
	v_pk_add_f32 v[36:37], v[40:41], v[88:89] neg_hi:[0,1]
	v_pk_add_f32 v[38:39], v[40:41], v[88:89] neg_lo:[0,1]
	v_pk_add_f32 v[88:89], v[68:69], v[86:87] neg_hi:[0,1]
	v_pk_add_f32 v[68:69], v[68:69], v[86:87] neg_lo:[0,1]
	v_cvt_f32_fp8_sdwa v91, v76 src0_sel:BYTE_3
	v_pk_mul_f32 v[42:43], v[36:37], v[38:39] op_sel:[0,0] op_sel_hi:[0,1]
	v_pk_fma_f32 v[42:43], v[36:37], v[38:39], v[42:43] op_sel:[1,1,0] op_sel_hi:[1,0,1] neg_hi:[0,1,0]
	ds_read2_b64 v[36:39], v92 offset0:2 offset1:3
	v_pk_mul_f32 v[40:41], v[88:89], v[68:69] op_sel:[0,0] op_sel_hi:[0,1]
	v_pk_fma_f32 v[40:41], v[88:89], v[68:69], v[40:41] op_sel:[1,1,0] op_sel_hi:[1,0,1] neg_hi:[0,1,0]
	ds_read2_b64 v[86:89], v92 offset1:1
	s_waitcnt lgkmcnt(1)
	v_pk_add_f32 v[68:69], v[32:33], v[38:39] neg_hi:[0,1]
	v_pk_add_f32 v[32:33], v[32:33], v[38:39] neg_lo:[0,1]
	v_cvt_f32_fp8_sdwa v76, v75 src0_sel:BYTE_1
	v_pk_mul_f32 v[38:39], v[68:69], v[32:33] op_sel:[0,0] op_sel_hi:[0,1]
	v_pk_fma_f32 v[38:39], v[68:69], v[32:33], v[38:39] op_sel:[1,1,0] op_sel_hi:[1,0,1] neg_hi:[0,1,0]
	v_pk_add_f32 v[32:33], v[34:35], v[36:37] neg_hi:[0,1]
	v_pk_add_f32 v[34:35], v[34:35], v[36:37] neg_lo:[0,1]
	v_cvt_f32_fp8_sdwa v68, v83 src0_sel:BYTE_1
	v_pk_mul_f32 v[36:37], v[32:33], v[34:35] op_sel:[0,0] op_sel_hi:[0,1]
	v_pk_fma_f32 v[36:37], v[32:33], v[34:35], v[36:37] op_sel:[1,1,0] op_sel_hi:[1,0,1] neg_hi:[0,1,0]
	s_waitcnt lgkmcnt(0)
	v_pk_add_f32 v[32:33], v[64:65], v[88:89] neg_hi:[0,1]
	v_pk_add_f32 v[64:65], v[64:65], v[88:89] neg_lo:[0,1]
	v_cvt_f32_fp8_sdwa v69, v83 src0_sel:BYTE_3
	v_pk_mul_f32 v[34:35], v[32:33], v[64:65] op_sel:[0,0] op_sel_hi:[0,1]
	v_pk_fma_f32 v[34:35], v[32:33], v[64:65], v[34:35] op_sel:[1,1,0] op_sel_hi:[1,0,1] neg_hi:[0,1,0]
	v_pk_add_f32 v[64:65], v[66:67], v[86:87] neg_hi:[0,1]
	v_pk_add_f32 v[66:67], v[66:67], v[86:87] neg_lo:[0,1]
	v_cvt_f32_fp8_sdwa v83, v81 src0_sel:BYTE_3
	v_pk_mul_f32 v[32:33], v[64:65], v[66:67] op_sel:[0,0] op_sel_hi:[0,1]
	v_pk_fma_f32 v[32:33], v[64:65], v[66:67], v[32:33] op_sel:[1,1,0] op_sel_hi:[1,0,1] neg_hi:[0,1,0]
	v_cvt_f32_fp8_sdwa v64, v85 src0_sel:BYTE_1
	v_cvt_f32_fp8_sdwa v65, v85 src0_sel:BYTE_3
	v_cvt_f32_fp8_sdwa v66, v84 src0_sel:BYTE_1
	v_cvt_f32_fp8_sdwa v67, v84 src0_sel:BYTE_3
	v_cvt_f32_fp8_sdwa v84, v82 src0_sel:BYTE_1
	v_cvt_f32_fp8_sdwa v85, v82 src0_sel:BYTE_3
	v_cvt_f32_fp8_sdwa v82, v81 src0_sel:BYTE_1
	v_cvt_f32_fp8_sdwa v86, v80 src0_sel:BYTE_1
	v_cvt_f32_fp8_sdwa v87, v80 src0_sel:BYTE_3
	v_cvt_f32_fp8_sdwa v80, v79 src0_sel:BYTE_1
	v_cvt_f32_fp8_sdwa v81, v79 src0_sel:BYTE_3
	v_cvt_f32_fp8_sdwa v88, v78 src0_sel:BYTE_1
	v_cvt_f32_fp8_sdwa v89, v78 src0_sel:BYTE_3
	v_cvt_f32_fp8_sdwa v78, v77 src0_sel:BYTE_1
	v_cvt_f32_fp8_sdwa v79, v77 src0_sel:BYTE_3
	v_cvt_f32_fp8_sdwa v77, v75 src0_sel:BYTE_3
	v_cvt_f32_fp8_sdwa v92, v74 src0_sel:BYTE_1
	v_cvt_f32_fp8_sdwa v74, v73 src0_sel:BYTE_1
	v_cvt_f32_fp8_sdwa v75, v73 src0_sel:BYTE_3
	v_cvt_f32_fp8_sdwa v73, v71 src0_sel:BYTE_3
	v_pk_add_f32 v[70:71], v[64:65], v[78:79]
	v_pk_add_f32 v[64:65], v[64:65], v[78:79] neg_lo:[0,1] neg_hi:[0,1]
	v_pk_add_f32 v[78:79], v[82:83], v[74:75]
	v_pk_add_f32 v[74:75], v[82:83], v[74:75] neg_lo:[0,1] neg_hi:[0,1]
	v_pk_add_f32 v[82:83], v[70:71], v[78:79]
	v_pk_add_f32 v[70:71], v[70:71], v[78:79] neg_lo:[0,1] neg_hi:[0,1]
	v_pk_add_f32 v[78:79], v[64:65], v[74:75] op_sel:[0,1] op_sel_hi:[1,0] neg_hi:[0,1]
	v_pk_add_f32 v[64:65], v[64:65], v[74:75] op_sel:[0,1] op_sel_hi:[1,0] neg_lo:[0,1]
	v_pk_add_f32 v[74:75], v[66:67], v[90:91]
	v_pk_add_f32 v[66:67], v[66:67], v[90:91] neg_lo:[0,1] neg_hi:[0,1]
	v_pk_add_f32 v[90:91], v[86:87], v[94:95]
	v_pk_add_f32 v[86:87], v[86:87], v[94:95] neg_lo:[0,1] neg_hi:[0,1]
	v_pk_add_f32 v[94:95], v[74:75], v[90:91]
	v_pk_add_f32 v[74:75], v[74:75], v[90:91] neg_lo:[0,1] neg_hi:[0,1]
	v_pk_add_f32 v[90:91], v[66:67], v[86:87] op_sel:[0,1] op_sel_hi:[1,0] neg_hi:[0,1]
	v_pk_add_f32 v[66:67], v[66:67], v[86:87] op_sel:[0,1] op_sel_hi:[1,0] neg_lo:[0,1]
	v_pk_add_f32 v[86:87], v[68:69], v[76:77]
	v_pk_add_f32 v[68:69], v[68:69], v[76:77] neg_lo:[0,1] neg_hi:[0,1]
	v_pk_add_f32 v[76:77], v[80:81], v[72:73]
	v_pk_add_f32 v[72:73], v[80:81], v[72:73] neg_lo:[0,1] neg_hi:[0,1]
	v_pk_add_f32 v[80:81], v[86:87], v[76:77]
	v_pk_add_f32 v[76:77], v[86:87], v[76:77] neg_lo:[0,1] neg_hi:[0,1]
	v_pk_add_f32 v[86:87], v[68:69], v[72:73] op_sel:[0,1] op_sel_hi:[1,0] neg_hi:[0,1]
	v_pk_add_f32 v[68:69], v[68:69], v[72:73] op_sel:[0,1] op_sel_hi:[1,0] neg_lo:[0,1]
	v_pk_add_f32 v[72:73], v[84:85], v[92:93]
	v_pk_add_f32 v[84:85], v[84:85], v[92:93] neg_lo:[0,1] neg_hi:[0,1]
	v_pk_add_f32 v[92:93], v[88:89], v[98:99]
	v_pk_add_f32 v[88:89], v[88:89], v[98:99] neg_lo:[0,1] neg_hi:[0,1]
	v_pk_add_f32 v[98:99], v[72:73], v[92:93]
	v_pk_add_f32 v[72:73], v[72:73], v[92:93] neg_lo:[0,1] neg_hi:[0,1]
	v_pk_add_f32 v[92:93], v[84:85], v[88:89] op_sel:[0,1] op_sel_hi:[1,0] neg_hi:[0,1]
	v_pk_add_f32 v[84:85], v[84:85], v[88:89] op_sel:[0,1] op_sel_hi:[1,0] neg_lo:[0,1]
	v_pk_mul_f32 v[88:89], v[90:91], s[6:7] op_sel:[0,0] op_sel_hi:[0,1]
	v_pk_fma_f32 v[88:89], v[90:91], s[6:7], v[88:89] op_sel:[1,1,0] op_sel_hi:[1,0,1] neg_lo:[0,1,0]
	v_pk_mul_f32 v[90:91], v[66:67], s[10:11] op_sel:[0,0] op_sel_hi:[0,1]
	v_pk_fma_f32 v[90:91], v[66:67], s[10:11], v[90:91] op_sel:[1,1,0] op_sel_hi:[1,0,1] neg_lo:[0,1,0]
	v_pk_add_f32 v[66:67], v[86:87], v[86:87] op_sel:[0,1] op_sel_hi:[1,0] neg_hi:[0,1]
	s_nop 0
	v_pk_add_f32 v[72:73], v[72:73], v[72:73] op_sel:[0,1] op_sel_hi:[1,0] neg_lo:[0,1]
	v_pk_mul_f32 v[86:87], v[92:93], s[10:11] op_sel:[0,0] op_sel_hi:[0,1]
	v_pk_fma_f32 v[86:87], v[92:93], s[10:11], v[86:87] op_sel:[1,1,0] op_sel_hi:[1,0,1] neg_lo:[0,1,0]
	s_mov_b32 s14, s11
	v_pk_mul_f32 v[66:67], v[66:67], s[8:9]
	s_mov_b32 s15, s10
	v_pk_mul_f32 v[92:93], v[84:85], s[14:15] op_sel:[0,0] op_sel_hi:[0,1]
	v_pk_fma_f32 v[92:93], v[84:85], s[14:15], v[92:93] op_sel:[1,1,0] op_sel_hi:[1,0,1] neg_lo:[0,1,0]
	v_pk_add_f32 v[84:85], v[82:83], v[80:81]
	v_pk_add_f32 v[80:81], v[82:83], v[80:81] neg_lo:[0,1] neg_hi:[0,1]
	v_pk_add_f32 v[82:83], v[94:95], v[98:99]
	v_pk_add_f32 v[94:95], v[94:95], v[98:99] neg_lo:[0,1] neg_hi:[0,1]
	v_pk_add_f32 v[74:75], v[74:75], v[74:75] op_sel:[0,1] op_sel_hi:[1,0] neg_hi:[0,1]
	v_pk_add_f32 v[68:69], v[68:69], v[68:69] op_sel:[0,1] op_sel_hi:[1,0] neg_lo:[0,1]
	s_mov_b32 s13, s12
	v_pk_mul_f32 v[72:73], v[72:73], s[12:13]
	v_pk_add_f32 v[98:99], v[84:85], v[82:83]
	v_pk_add_f32 v[82:83], v[84:85], v[82:83] neg_lo:[0,1] neg_hi:[0,1]
	v_pk_add_f32 v[84:85], v[80:81], v[94:95] op_sel:[0,1] op_sel_hi:[1,0] neg_hi:[0,1]
	v_pk_add_f32 v[80:81], v[80:81], v[94:95] op_sel:[0,1] op_sel_hi:[1,0] neg_lo:[0,1]
	v_pk_add_f32 v[94:95], v[78:79], v[66:67]
	v_pk_add_f32 v[66:67], v[78:79], v[66:67] neg_lo:[0,1] neg_hi:[0,1]
	v_pk_add_f32 v[78:79], v[88:89], v[86:87]
	v_pk_add_f32 v[86:87], v[88:89], v[86:87] neg_lo:[0,1] neg_hi:[0,1]
	v_pk_mul_f32 v[74:75], v[74:75], s[8:9]
	v_pk_mul_f32 v[68:69], v[68:69], s[12:13]
	v_pk_add_f32 v[88:89], v[94:95], v[78:79]
	v_pk_add_f32 v[78:79], v[94:95], v[78:79] neg_lo:[0,1] neg_hi:[0,1]
	v_pk_add_f32 v[94:95], v[66:67], v[86:87] op_sel:[0,1] op_sel_hi:[1,0] neg_hi:[0,1]
	v_pk_add_f32 v[66:67], v[66:67], v[86:87] op_sel:[0,1] op_sel_hi:[1,0] neg_lo:[0,1]
	v_pk_add_f32 v[86:87], v[70:71], v[76:77] op_sel:[0,1] op_sel_hi:[1,0] neg_hi:[0,1]
	v_pk_add_f32 v[70:71], v[70:71], v[76:77] op_sel:[0,1] op_sel_hi:[1,0] neg_lo:[0,1]
	v_pk_add_f32 v[76:77], v[74:75], v[72:73]
	v_pk_add_f32 v[72:73], v[74:75], v[72:73] neg_lo:[0,1] neg_hi:[0,1]
	v_pk_add_f32 v[74:75], v[76:77], v[86:87]
	v_pk_add_f32 v[76:77], v[86:87], v[76:77] neg_lo:[0,1] neg_hi:[0,1]
	v_pk_add_f32 v[86:87], v[70:71], v[72:73] op_sel:[0,1] op_sel_hi:[1,0] neg_hi:[0,1]
	v_pk_add_f32 v[70:71], v[70:71], v[72:73] op_sel:[0,1] op_sel_hi:[1,0] neg_lo:[0,1]
	v_pk_add_f32 v[72:73], v[64:65], v[68:69]
	v_pk_add_f32 v[64:65], v[64:65], v[68:69] neg_lo:[0,1] neg_hi:[0,1]
	v_pk_add_f32 v[68:69], v[90:91], v[92:93]
	v_pk_add_f32 v[90:91], v[90:91], v[92:93] neg_lo:[0,1] neg_hi:[0,1]
	v_pk_add_f32 v[92:93], v[72:73], v[68:69]
	v_pk_add_f32 v[68:69], v[72:73], v[68:69] neg_lo:[0,1] neg_hi:[0,1]
	v_pk_add_f32 v[72:73], v[64:65], v[90:91] op_sel:[0,1] op_sel_hi:[1,0] neg_hi:[0,1]
	v_pk_add_f32 v[64:65], v[64:65], v[90:91] op_sel:[0,1] op_sel_hi:[1,0] neg_lo:[0,1]
	v_pk_mul_f32 v[90:91], v[88:89], v[30:31] op_sel:[0,0] op_sel_hi:[0,1]
	v_pk_fma_f32 v[90:91], v[88:89], v[30:31], v[90:91] op_sel:[1,1,0] op_sel_hi:[1,0,1] neg_lo:[0,1,0]
	v_pk_mul_f32 v[88:89], v[74:75], v[28:29] op_sel:[0,0] op_sel_hi:[0,1]
	v_pk_fma_f32 v[88:89], v[74:75], v[28:29], v[88:89] op_sel:[1,1,0] op_sel_hi:[1,0,1] neg_lo:[0,1,0]
	v_pk_mul_f32 v[74:75], v[92:93], v[26:27] op_sel:[0,0] op_sel_hi:[0,1]
	v_pk_fma_f32 v[74:75], v[92:93], v[26:27], v[74:75] op_sel:[1,1,0] op_sel_hi:[1,0,1] neg_lo:[0,1,0]
	s_barrier
	ds_write_b64 v1, v[74:75] offset:6552
	v_pk_mul_f32 v[74:75], v[84:85], v[24:25] op_sel:[0,0] op_sel_hi:[0,1]
	v_pk_fma_f32 v[74:75], v[84:85], v[24:25], v[74:75] op_sel:[1,1,0] op_sel_hi:[1,0,1] neg_lo:[0,1,0]
	ds_write_b64 v1, v[74:75] offset:8736
	v_pk_mul_f32 v[74:75], v[94:95], v[20:21] op_sel:[0,0] op_sel_hi:[0,1]
	v_pk_fma_f32 v[74:75], v[94:95], v[20:21], v[74:75] op_sel:[1,1,0] op_sel_hi:[1,0,1] neg_lo:[0,1,0]
	ds_write_b64 v1, v[74:75] offset:10920
	v_pk_mul_f32 v[74:75], v[86:87], v[16:17] op_sel:[0,0] op_sel_hi:[0,1]
	v_pk_fma_f32 v[74:75], v[86:87], v[16:17], v[74:75] op_sel:[1,1,0] op_sel_hi:[1,0,1] neg_lo:[0,1,0]
	ds_write_b64 v1, v[74:75] offset:13104
	v_pk_mul_f32 v[74:75], v[72:73], v[10:11] op_sel:[0,0] op_sel_hi:[0,1]
	v_pk_fma_f32 v[74:75], v[72:73], v[10:11], v[74:75] op_sel:[1,1,0] op_sel_hi:[1,0,1] neg_lo:[0,1,0]
	v_pk_mul_f32 v[72:73], v[82:83], v[22:23] op_sel:[0,0] op_sel_hi:[0,1]
	v_pk_fma_f32 v[72:73], v[82:83], v[22:23], v[72:73] op_sel:[1,1,0] op_sel_hi:[1,0,1] neg_lo:[0,1,0]
	ds_write_b64 v1, v[72:73] offset:17472
	v_pk_mul_f32 v[72:73], v[78:79], v[18:19] op_sel:[0,0] op_sel_hi:[0,1]
	v_pk_fma_f32 v[72:73], v[78:79], v[18:19], v[72:73] op_sel:[1,1,0] op_sel_hi:[1,0,1] neg_lo:[0,1,0]
	ds_write_b64 v1, v[72:73] offset:19656
	v_pk_mul_f32 v[72:73], v[76:77], v[12:13] op_sel:[0,0] op_sel_hi:[0,1]
	v_pk_fma_f32 v[72:73], v[76:77], v[12:13], v[72:73] op_sel:[1,1,0] op_sel_hi:[1,0,1] neg_lo:[0,1,0]
	ds_write_b64 v1, v[72:73] offset:21840
	v_pk_mul_f32 v[72:73], v[68:69], v[14:15] op_sel:[0,0] op_sel_hi:[0,1]
	v_pk_fma_f32 v[72:73], v[68:69], v[14:15], v[72:73] op_sel:[1,1,0] op_sel_hi:[1,0,1] neg_lo:[0,1,0]
	v_pk_mul_f32 v[68:69], v[80:81], v[6:7] op_sel:[0,0] op_sel_hi:[0,1]
	v_pk_fma_f32 v[68:69], v[80:81], v[6:7], v[68:69] op_sel:[1,1,0] op_sel_hi:[1,0,1] neg_lo:[0,1,0]
	ds_write_b64 v1, v[68:69] offset:26208
	v_pk_mul_f32 v[68:69], v[66:67], v[8:9] op_sel:[0,0] op_sel_hi:[0,1]
	v_pk_fma_f32 v[68:69], v[66:67], v[8:9], v[68:69] op_sel:[1,1,0] op_sel_hi:[1,0,1] neg_lo:[0,1,0]
	v_pk_mul_f32 v[66:67], v[70:71], v[4:5] op_sel:[0,0] op_sel_hi:[0,1]
	v_pk_fma_f32 v[66:67], v[70:71], v[4:5], v[66:67] op_sel:[1,1,0] op_sel_hi:[1,0,1] neg_lo:[0,1,0]
	ds_write_b64 v1, v[66:67] offset:30576
	v_pk_mul_f32 v[66:67], v[64:65], v[2:3] op_sel:[0,0] op_sel_hi:[0,1]
	v_pk_fma_f32 v[66:67], v[64:65], v[2:3], v[66:67] op_sel:[1,1,0] op_sel_hi:[1,0,1] neg_lo:[0,1,0]
	ds_write_b64 v1, v[98:99]
	ds_write_b64 v1, v[90:91] offset:2184
	ds_write_b64 v1, v[88:89] offset:4368
	ds_write_b64 v1, v[74:75] offset:15288
	ds_write_b64 v1, v[72:73] offset:24024
	ds_write_b64 v1, v[68:69] offset:28392
	ds_write_b64 v1, v[66:67] offset:32760
	s_waitcnt lgkmcnt(0)
	s_barrier
	ds_read2_b64 v[64:67], v96 offset1:16
	ds_read2_b64 v[68:71], v96 offset0:32 offset1:48
	ds_read2_b64 v[72:75], v96 offset0:64 offset1:80
	ds_read2_b64 v[76:79], v96 offset0:128 offset1:144
	ds_read2_b64 v[80:83], v96 offset0:96 offset1:112
	ds_read2_b64 v[84:87], v96 offset0:192 offset1:208
	ds_read2_b64 v[88:91], v96 offset0:160 offset1:176
	ds_read2_b64 v[92:95], v96 offset0:224 offset1:240
	s_waitcnt lgkmcnt(4)
	v_pk_add_f32 v[98:99], v[64:65], v[76:77]
	v_pk_add_f32 v[64:65], v[64:65], v[76:77] neg_lo:[0,1] neg_hi:[0,1]
	s_waitcnt lgkmcnt(2)
	v_pk_add_f32 v[76:77], v[72:73], v[84:85]
	v_pk_add_f32 v[72:73], v[72:73], v[84:85] neg_lo:[0,1] neg_hi:[0,1]
	v_pk_add_f32 v[84:85], v[98:99], v[76:77]
	v_pk_add_f32 v[76:77], v[98:99], v[76:77] neg_lo:[0,1] neg_hi:[0,1]
	v_pk_add_f32 v[98:99], v[64:65], v[72:73] op_sel:[0,1] op_sel_hi:[1,0] neg_hi:[0,1]
	v_pk_add_f32 v[64:65], v[64:65], v[72:73] op_sel:[0,1] op_sel_hi:[1,0] neg_lo:[0,1]
	v_pk_add_f32 v[72:73], v[66:67], v[78:79]
	v_pk_add_f32 v[66:67], v[66:67], v[78:79] neg_lo:[0,1] neg_hi:[0,1]
	v_pk_add_f32 v[78:79], v[74:75], v[86:87]
	v_pk_add_f32 v[74:75], v[74:75], v[86:87] neg_lo:[0,1] neg_hi:[0,1]
	v_pk_add_f32 v[86:87], v[72:73], v[78:79]
	v_pk_add_f32 v[72:73], v[72:73], v[78:79] neg_lo:[0,1] neg_hi:[0,1]
	v_pk_add_f32 v[78:79], v[66:67], v[74:75] op_sel:[0,1] op_sel_hi:[1,0] neg_hi:[0,1]
	v_pk_add_f32 v[66:67], v[66:67], v[74:75] op_sel:[0,1] op_sel_hi:[1,0] neg_lo:[0,1]
	s_waitcnt lgkmcnt(1)
	v_pk_add_f32 v[74:75], v[68:69], v[88:89]
	v_pk_add_f32 v[68:69], v[68:69], v[88:89] neg_lo:[0,1] neg_hi:[0,1]
	s_waitcnt lgkmcnt(0)
	v_pk_add_f32 v[88:89], v[80:81], v[92:93]
	v_pk_add_f32 v[80:81], v[80:81], v[92:93] neg_lo:[0,1] neg_hi:[0,1]
	v_pk_add_f32 v[92:93], v[74:75], v[88:89]
	v_pk_add_f32 v[74:75], v[74:75], v[88:89] neg_lo:[0,1] neg_hi:[0,1]
	v_pk_add_f32 v[88:89], v[68:69], v[80:81] op_sel:[0,1] op_sel_hi:[1,0] neg_hi:[0,1]
	v_pk_add_f32 v[68:69], v[68:69], v[80:81] op_sel:[0,1] op_sel_hi:[1,0] neg_lo:[0,1]
	v_pk_add_f32 v[80:81], v[70:71], v[90:91]
	v_pk_add_f32 v[70:71], v[70:71], v[90:91] neg_lo:[0,1] neg_hi:[0,1]
	v_pk_add_f32 v[90:91], v[82:83], v[94:95]
	v_pk_add_f32 v[82:83], v[82:83], v[94:95] neg_lo:[0,1] neg_hi:[0,1]
	v_pk_add_f32 v[94:95], v[80:81], v[90:91]
	v_pk_add_f32 v[80:81], v[80:81], v[90:91] neg_lo:[0,1] neg_hi:[0,1]
	v_pk_add_f32 v[90:91], v[70:71], v[82:83] op_sel:[0,1] op_sel_hi:[1,0] neg_hi:[0,1]
	v_pk_add_f32 v[70:71], v[70:71], v[82:83] op_sel:[0,1] op_sel_hi:[1,0] neg_lo:[0,1]
	v_pk_mul_f32 v[82:83], v[78:79], s[6:7] op_sel:[0,0] op_sel_hi:[0,1]
	v_pk_fma_f32 v[82:83], v[78:79], s[6:7], v[82:83] op_sel:[1,1,0] op_sel_hi:[1,0,1] neg_lo:[0,1,0]
	v_pk_mul_f32 v[78:79], v[66:67], s[10:11] op_sel:[0,0] op_sel_hi:[0,1]
	v_pk_fma_f32 v[78:79], v[66:67], s[10:11], v[78:79] op_sel:[1,1,0] op_sel_hi:[1,0,1] neg_lo:[0,1,0]
	v_pk_add_f32 v[66:67], v[88:89], v[88:89] op_sel:[0,1] op_sel_hi:[1,0] neg_hi:[0,1]
	v_pk_add_f32 v[72:73], v[72:73], v[72:73] op_sel:[0,1] op_sel_hi:[1,0] neg_hi:[0,1]
	s_nop 0
	v_pk_mul_f32 v[88:89], v[90:91], s[10:11] op_sel:[0,0] op_sel_hi:[0,1]
	v_pk_fma_f32 v[88:89], v[90:91], s[10:11], v[88:89] op_sel:[1,1,0] op_sel_hi:[1,0,1] neg_lo:[0,1,0]
	v_pk_mul_f32 v[90:91], v[70:71], s[14:15] op_sel:[0,0] op_sel_hi:[0,1]
	v_pk_fma_f32 v[90:91], v[70:71], s[14:15], v[90:91] op_sel:[1,1,0] op_sel_hi:[1,0,1] neg_lo:[0,1,0]
	v_pk_add_f32 v[70:71], v[84:85], v[92:93]
	v_pk_mul_f32 v[66:67], v[66:67], s[8:9]
	v_pk_add_f32 v[84:85], v[84:85], v[92:93] neg_lo:[0,1] neg_hi:[0,1]
	v_pk_add_f32 v[92:93], v[86:87], v[94:95]
	v_pk_add_f32 v[86:87], v[86:87], v[94:95] neg_lo:[0,1] neg_hi:[0,1]
	v_pk_add_f32 v[68:69], v[68:69], v[68:69] op_sel:[0,1] op_sel_hi:[1,0] neg_lo:[0,1]
	v_pk_add_f32 v[80:81], v[80:81], v[80:81] op_sel:[0,1] op_sel_hi:[1,0] neg_lo:[0,1]
	v_pk_add_f32 v[94:95], v[70:71], v[92:93]
	v_pk_add_f32 v[92:93], v[70:71], v[92:93] neg_lo:[0,1] neg_hi:[0,1]
	v_pk_add_f32 v[100:101], v[84:85], v[86:87] op_sel:[0,1] op_sel_hi:[1,0] neg_hi:[0,1]
	v_pk_add_f32 v[84:85], v[84:85], v[86:87] op_sel:[0,1] op_sel_hi:[1,0] neg_lo:[0,1]
	v_pk_add_f32 v[70:71], v[98:99], v[66:67]
	v_pk_add_f32 v[66:67], v[98:99], v[66:67] neg_lo:[0,1] neg_hi:[0,1]
	v_pk_add_f32 v[86:87], v[82:83], v[88:89]
	v_pk_add_f32 v[82:83], v[82:83], v[88:89] neg_lo:[0,1] neg_hi:[0,1]
	v_pk_mul_f32 v[72:73], v[72:73], s[8:9]
	v_pk_mul_f32 v[68:69], v[68:69], s[12:13]
	v_pk_mul_f32 v[80:81], v[80:81], s[12:13]
	v_pk_add_f32 v[88:89], v[70:71], v[86:87]
	v_pk_add_f32 v[86:87], v[70:71], v[86:87] neg_lo:[0,1] neg_hi:[0,1]
	v_pk_add_f32 v[98:99], v[66:67], v[82:83] op_sel:[0,1] op_sel_hi:[1,0] neg_hi:[0,1]
	v_pk_add_f32 v[82:83], v[66:67], v[82:83] op_sel:[0,1] op_sel_hi:[1,0] neg_lo:[0,1]
	v_pk_add_f32 v[66:67], v[76:77], v[74:75] op_sel:[0,1] op_sel_hi:[1,0] neg_hi:[0,1]
	v_pk_add_f32 v[70:71], v[76:77], v[74:75] op_sel:[0,1] op_sel_hi:[1,0] neg_lo:[0,1]
	v_pk_add_f32 v[74:75], v[72:73], v[80:81]
	v_pk_add_f32 v[72:73], v[72:73], v[80:81] neg_lo:[0,1] neg_hi:[0,1]
	v_pk_add_f32 v[76:77], v[74:75], v[66:67]
	v_pk_add_f32 v[74:75], v[66:67], v[74:75] neg_lo:[0,1] neg_hi:[0,1]
	v_pk_add_f32 v[66:67], v[64:65], v[68:69]
	v_pk_add_f32 v[64:65], v[64:65], v[68:69] neg_lo:[0,1] neg_hi:[0,1]
	v_pk_add_f32 v[68:69], v[78:79], v[90:91]
	v_pk_add_f32 v[80:81], v[70:71], v[72:73] op_sel:[0,1] op_sel_hi:[1,0] neg_hi:[0,1]
	v_pk_add_f32 v[72:73], v[70:71], v[72:73] op_sel:[0,1] op_sel_hi:[1,0] neg_lo:[0,1]
	v_pk_add_f32 v[70:71], v[78:79], v[90:91] neg_lo:[0,1] neg_hi:[0,1]
	v_pk_add_f32 v[78:79], v[66:67], v[68:69]
	v_pk_add_f32 v[90:91], v[66:67], v[68:69] neg_lo:[0,1] neg_hi:[0,1]
	v_mov_b32_e32 v68, v0
	v_pk_add_f32 v[102:103], v[64:65], v[70:71] op_sel:[0,1] op_sel_hi:[1,0] neg_hi:[0,1]
	v_pk_add_f32 v[104:105], v[64:65], v[70:71] op_sel:[0,1] op_sel_hi:[1,0] neg_lo:[0,1]
	s_nop 0
	v_ashrrev_i32_e32 v64, 4, v68
	v_lshlrev_b32_e32 v97, 3, v64
	v_add_u32_e32 v108, 0x8800, v97
	v_and_b32_e32 v68, 15, v68
	ds_read2_b64 v[64:67], v108 offset0:16 offset1:32
	v_mad_u32_u24 v109, v68, s5, v97
	ds_read2_b64 v[68:71], v108 offset0:48 offset1:64
	s_waitcnt lgkmcnt(1)
	v_pk_mul_f32 v[106:107], v[88:89], v[64:65] op_sel:[0,0] op_sel_hi:[0,1]
	v_pk_fma_f32 v[106:107], v[88:89], v[64:65], v[106:107] op_sel:[1,1,0] op_sel_hi:[1,0,1] neg_lo:[0,1,0]
	v_pk_mul_f32 v[88:89], v[76:77], v[66:67] op_sel:[0,0] op_sel_hi:[0,1]
	v_pk_fma_f32 v[88:89], v[76:77], v[66:67], v[88:89] op_sel:[1,1,0] op_sel_hi:[1,0,1] neg_lo:[0,1,0]
	s_waitcnt lgkmcnt(0)
	v_pk_mul_f32 v[76:77], v[78:79], v[68:69] op_sel:[0,0] op_sel_hi:[0,1]
	v_pk_fma_f32 v[76:77], v[78:79], v[68:69], v[76:77] op_sel:[1,1,0] op_sel_hi:[1,0,1] neg_lo:[0,1,0]
	ds_write2_b64 v109, v[88:89], v[76:77] offset0:32 offset1:48
	v_pk_mul_f32 v[76:77], v[100:101], v[70:71] op_sel:[0,0] op_sel_hi:[0,1]
	v_pk_fma_f32 v[76:77], v[100:101], v[70:71], v[76:77] op_sel:[1,1,0] op_sel_hi:[1,0,1] neg_lo:[0,1,0]
	ds_read2_b64 v[64:67], v108 offset0:80 offset1:96
	s_waitcnt lgkmcnt(0)
	v_pk_mul_f32 v[78:79], v[98:99], v[64:65] op_sel:[0,0] op_sel_hi:[0,1]
	v_pk_fma_f32 v[78:79], v[98:99], v[64:65], v[78:79] op_sel:[1,1,0] op_sel_hi:[1,0,1] neg_lo:[0,1,0]
	ds_write2_b64 v109, v[76:77], v[78:79] offset0:64 offset1:80
	v_pk_mul_f32 v[76:77], v[80:81], v[66:67] op_sel:[0,0] op_sel_hi:[0,1]
	v_pk_fma_f32 v[76:77], v[80:81], v[66:67], v[76:77] op_sel:[1,1,0] op_sel_hi:[1,0,1] neg_lo:[0,1,0]
	ds_read2_b64 v[68:71], v108 offset0:112 offset1:128
	ds_read2_b64 v[64:67], v108 offset0:144 offset1:160
	s_waitcnt lgkmcnt(1)
	v_pk_mul_f32 v[78:79], v[102:103], v[68:69] op_sel:[0,0] op_sel_hi:[0,1]
	v_pk_fma_f32 v[78:79], v[102:103], v[68:69], v[78:79] op_sel:[1,1,0] op_sel_hi:[1,0,1] neg_lo:[0,1,0]
	ds_write2_b64 v109, v[76:77], v[78:79] offset0:96 offset1:112
	v_pk_mul_f32 v[76:77], v[92:93], v[70:71] op_sel:[0,0] op_sel_hi:[0,1]
	v_pk_fma_f32 v[76:77], v[92:93], v[70:71], v[76:77] op_sel:[1,1,0] op_sel_hi:[1,0,1] neg_lo:[0,1,0]
	ds_read2_b64 v[68:71], v108 offset0:176 offset1:192
	s_waitcnt lgkmcnt(2)
	v_pk_mul_f32 v[78:79], v[86:87], v[64:65] op_sel:[0,0] op_sel_hi:[0,1]
	v_pk_fma_f32 v[78:79], v[86:87], v[64:65], v[78:79] op_sel:[1,1,0] op_sel_hi:[1,0,1] neg_lo:[0,1,0]
	ds_write2_b64 v109, v[76:77], v[78:79] offset0:128 offset1:144
	v_pk_mul_f32 v[76:77], v[74:75], v[66:67] op_sel:[0,0] op_sel_hi:[0,1]
	v_pk_fma_f32 v[76:77], v[74:75], v[66:67], v[76:77] op_sel:[1,1,0] op_sel_hi:[1,0,1] neg_lo:[0,1,0]
	ds_read2_b64 v[64:67], v108 offset0:208 offset1:224
	s_waitcnt lgkmcnt(2)
	v_pk_mul_f32 v[74:75], v[90:91], v[68:69] op_sel:[0,0] op_sel_hi:[0,1]
	v_pk_fma_f32 v[74:75], v[90:91], v[68:69], v[74:75] op_sel:[1,1,0] op_sel_hi:[1,0,1] neg_lo:[0,1,0]
	ds_write2_b64 v109, v[76:77], v[74:75] offset0:160 offset1:176
	v_pk_mul_f32 v[74:75], v[84:85], v[70:71] op_sel:[0,0] op_sel_hi:[0,1]
	v_pk_fma_f32 v[74:75], v[84:85], v[70:71], v[74:75] op_sel:[1,1,0] op_sel_hi:[1,0,1] neg_lo:[0,1,0]
	s_waitcnt lgkmcnt(1)
	v_pk_mul_f32 v[70:71], v[82:83], v[64:65] op_sel:[0,0] op_sel_hi:[0,1]
	v_pk_fma_f32 v[70:71], v[82:83], v[64:65], v[70:71] op_sel:[1,1,0] op_sel_hi:[1,0,1] neg_lo:[0,1,0]
	v_pk_mul_f32 v[64:65], v[72:73], v[66:67] op_sel:[0,0] op_sel_hi:[0,1]
	v_pk_fma_f32 v[64:65], v[72:73], v[66:67], v[64:65] op_sel:[1,1,0] op_sel_hi:[1,0,1] neg_lo:[0,1,0]
	ds_read_b64 v[68:69], v97 offset:36736
	s_waitcnt lgkmcnt(0)
	v_pk_mul_f32 v[66:67], v[104:105], v[68:69] op_sel:[0,0] op_sel_hi:[0,1]
	v_pk_fma_f32 v[66:67], v[104:105], v[68:69], v[66:67] op_sel:[1,1,0] op_sel_hi:[1,0,1] neg_lo:[0,1,0]
	ds_write2_b64 v109, v[64:65], v[66:67] offset0:224 offset1:240
	v_mov_b32_e32 v64, v0
	ds_write2_b64 v109, v[94:95], v[106:107] offset1:16
	ds_write2_b64 v109, v[74:75], v[70:71] offset0:192 offset1:208
	s_waitcnt lgkmcnt(0)
	s_barrier
	s_nop 0
	v_and_b32_e32 v65, 15, v64
	v_and_b32_e32 v64, 0x1ffffff0, v64
	v_lshlrev_b32_e32 v64, 3, v64
	v_mad_u32_u24 v92, v65, s5, v64
	ds_read2_b64 v[64:67], v92 offset1:1
	ds_read2_b64 v[68:71], v92 offset0:2 offset1:3
	ds_read2_b64 v[72:75], v92 offset0:8 offset1:9
	ds_read2_b64 v[76:79], v92 offset0:4 offset1:5
	ds_read2_b64 v[80:83], v92 offset0:6 offset1:7
	ds_read2_b64 v[84:87], v92 offset0:12 offset1:13
	ds_read2_b64 v[88:91], v92 offset0:10 offset1:11
	ds_read2_b64 v[92:95], v92 offset0:14 offset1:15
	s_waitcnt lgkmcnt(5)
	v_pk_add_f32 v[98:99], v[64:65], v[72:73]
	v_pk_add_f32 v[64:65], v[64:65], v[72:73] neg_lo:[0,1] neg_hi:[0,1]
	s_waitcnt lgkmcnt(2)
	v_pk_add_f32 v[72:73], v[76:77], v[84:85]
	v_pk_add_f32 v[76:77], v[76:77], v[84:85] neg_lo:[0,1] neg_hi:[0,1]
	v_pk_add_f32 v[84:85], v[98:99], v[72:73]
	v_pk_add_f32 v[98:99], v[98:99], v[72:73] neg_lo:[0,1] neg_hi:[0,1]
	v_pk_add_f32 v[100:101], v[64:65], v[76:77] op_sel:[0,1] op_sel_hi:[1,0] neg_hi:[0,1]
	v_pk_add_f32 v[102:103], v[64:65], v[76:77] op_sel:[0,1] op_sel_hi:[1,0] neg_lo:[0,1]
	v_pk_add_f32 v[64:65], v[66:67], v[74:75]
	v_pk_add_f32 v[72:73], v[78:79], v[86:87]
	v_pk_add_f32 v[66:67], v[66:67], v[74:75] neg_lo:[0,1] neg_hi:[0,1]
	v_pk_add_f32 v[74:75], v[78:79], v[86:87] neg_lo:[0,1] neg_hi:[0,1]
	v_pk_add_f32 v[76:77], v[64:65], v[72:73]
	v_pk_add_f32 v[64:65], v[64:65], v[72:73] neg_lo:[0,1] neg_hi:[0,1]
	v_pk_add_f32 v[72:73], v[66:67], v[74:75] op_sel:[0,1] op_sel_hi:[1,0] neg_hi:[0,1]
	v_pk_add_f32 v[66:67], v[66:67], v[74:75] op_sel:[0,1] op_sel_hi:[1,0] neg_lo:[0,1]
	s_waitcnt lgkmcnt(1)
	v_pk_add_f32 v[74:75], v[68:69], v[88:89]
	s_waitcnt lgkmcnt(0)
	v_pk_add_f32 v[78:79], v[80:81], v[92:93]
	v_pk_add_f32 v[64:65], v[64:65], v[64:65] op_sel:[0,1] op_sel_hi:[1,0] neg_hi:[0,1]
	v_pk_add_f32 v[68:69], v[68:69], v[88:89] neg_lo:[0,1] neg_hi:[0,1]
	v_pk_add_f32 v[80:81], v[80:81], v[92:93] neg_lo:[0,1] neg_hi:[0,1]
	v_pk_add_f32 v[86:87], v[74:75], v[78:79]
	v_pk_add_f32 v[78:79], v[74:75], v[78:79] neg_lo:[0,1] neg_hi:[0,1]
	v_pk_add_f32 v[74:75], v[68:69], v[80:81] op_sel:[0,1] op_sel_hi:[1,0] neg_hi:[0,1]
	v_pk_mul_f32 v[92:93], v[64:65], s[8:9]
	v_pk_add_f32 v[68:69], v[68:69], v[80:81] op_sel:[0,1] op_sel_hi:[1,0] neg_lo:[0,1]
	v_pk_add_f32 v[80:81], v[70:71], v[90:91]
	v_pk_add_f32 v[64:65], v[74:75], v[74:75] op_sel:[0,1] op_sel_hi:[1,0] neg_hi:[0,1]
	v_pk_add_f32 v[70:71], v[70:71], v[90:91] neg_lo:[0,1] neg_hi:[0,1]
	v_pk_add_f32 v[88:89], v[82:83], v[94:95]
	v_pk_add_f32 v[82:83], v[82:83], v[94:95] neg_lo:[0,1] neg_hi:[0,1]
	v_pk_mul_f32 v[94:95], v[66:67], s[10:11] op_sel:[0,0] op_sel_hi:[0,1]
	v_pk_fma_f32 v[94:95], v[66:67], s[10:11], v[94:95] op_sel:[1,1,0] op_sel_hi:[1,0,1] neg_lo:[0,1,0]
	v_pk_mul_f32 v[66:67], v[64:65], s[8:9]
	v_pk_add_f32 v[64:65], v[68:69], v[68:69] op_sel:[0,1] op_sel_hi:[1,0] neg_lo:[0,1]
	v_pk_add_f32 v[90:91], v[80:81], v[88:89]
	v_pk_add_f32 v[80:81], v[80:81], v[88:89] neg_lo:[0,1] neg_hi:[0,1]
	v_pk_add_f32 v[88:89], v[70:71], v[82:83] op_sel:[0,1] op_sel_hi:[1,0] neg_hi:[0,1]
	v_pk_add_f32 v[70:71], v[70:71], v[82:83] op_sel:[0,1] op_sel_hi:[1,0] neg_lo:[0,1]
	v_pk_mul_f32 v[104:105], v[64:65], s[12:13]
	v_pk_mul_f32 v[82:83], v[72:73], s[6:7] op_sel:[0,0] op_sel_hi:[0,1]
	v_pk_fma_f32 v[82:83], v[72:73], s[6:7], v[82:83] op_sel:[1,1,0] op_sel_hi:[1,0,1] neg_lo:[0,1,0]
	v_pk_add_f32 v[72:73], v[76:77], v[90:91]
	v_pk_add_f32 v[64:65], v[80:81], v[80:81] op_sel:[0,1] op_sel_hi:[1,0] neg_lo:[0,1]
	v_pk_mul_f32 v[68:69], v[88:89], s[10:11] op_sel:[0,0] op_sel_hi:[0,1]
	v_pk_fma_f32 v[68:69], v[88:89], s[10:11], v[68:69] op_sel:[1,1,0] op_sel_hi:[1,0,1] neg_lo:[0,1,0]
	v_pk_mul_f32 v[108:109], v[70:71], s[14:15] op_sel:[0,0] op_sel_hi:[0,1]
	v_pk_fma_f32 v[108:109], v[70:71], s[14:15], v[108:109] op_sel:[1,1,0] op_sel_hi:[1,0,1] neg_lo:[0,1,0]
	v_pk_add_f32 v[70:71], v[84:85], v[86:87] neg_lo:[0,1] neg_hi:[0,1]
	v_pk_mul_f32 v[106:107], v[64:65], s[12:13]
	v_pk_add_f32 v[64:65], v[84:85], v[86:87]
	v_pk_add_f32 v[74:75], v[76:77], v[90:91] neg_lo:[0,1] neg_hi:[0,1]
	v_pk_add_f32 v[88:89], v[64:65], v[72:73]
	v_pk_add_f32 v[72:73], v[64:65], v[72:73] neg_lo:[0,1] neg_hi:[0,1]
	v_pk_add_f32 v[80:81], v[70:71], v[74:75] op_sel:[0,1] op_sel_hi:[1,0] neg_hi:[0,1]
	v_pk_add_f32 v[64:65], v[70:71], v[74:75] op_sel:[0,1] op_sel_hi:[1,0] neg_lo:[0,1]
	v_pk_add_f32 v[70:71], v[100:101], v[66:67]
	v_pk_add_f32 v[66:67], v[100:101], v[66:67] neg_lo:[0,1] neg_hi:[0,1]
	v_pk_add_f32 v[74:75], v[82:83], v[68:69]
	v_pk_add_f32 v[68:69], v[82:83], v[68:69] neg_lo:[0,1] neg_hi:[0,1]
	v_pk_add_f32 v[90:91], v[70:71], v[74:75]
	v_pk_add_f32 v[74:75], v[70:71], v[74:75] neg_lo:[0,1] neg_hi:[0,1]
	v_pk_add_f32 v[82:83], v[66:67], v[68:69] op_sel:[0,1] op_sel_hi:[1,0] neg_hi:[0,1]
	v_pk_add_f32 v[66:67], v[66:67], v[68:69] op_sel:[0,1] op_sel_hi:[1,0] neg_lo:[0,1]
	v_pk_add_f32 v[68:69], v[98:99], v[78:79] op_sel:[0,1] op_sel_hi:[1,0] neg_hi:[0,1]
	v_pk_add_f32 v[70:71], v[98:99], v[78:79] op_sel:[0,1] op_sel_hi:[1,0] neg_lo:[0,1]
	v_pk_add_f32 v[76:77], v[92:93], v[106:107]
	v_pk_add_f32 v[78:79], v[92:93], v[106:107] neg_lo:[0,1] neg_hi:[0,1]
	v_pk_add_f32 v[92:93], v[76:77], v[68:69]
	v_pk_add_f32 v[76:77], v[68:69], v[76:77] neg_lo:[0,1] neg_hi:[0,1]
	v_pk_add_f32 v[86:87], v[70:71], v[78:79] op_sel:[0,1] op_sel_hi:[1,0] neg_hi:[0,1]
	v_pk_add_f32 v[68:69], v[70:71], v[78:79] op_sel:[0,1] op_sel_hi:[1,0] neg_lo:[0,1]
	v_pk_add_f32 v[70:71], v[102:103], v[104:105]
	v_pk_add_f32 v[98:99], v[102:103], v[104:105] neg_lo:[0,1] neg_hi:[0,1]
	v_pk_add_f32 v[78:79], v[94:95], v[108:109]
	v_pk_add_f32 v[100:101], v[94:95], v[108:109] neg_lo:[0,1] neg_hi:[0,1]
	v_pk_add_f32 v[94:95], v[70:71], v[78:79]
	v_pk_add_f32 v[78:79], v[70:71], v[78:79] neg_lo:[0,1] neg_hi:[0,1]
	v_pk_add_f32 v[84:85], v[98:99], v[100:101] op_sel:[0,1] op_sel_hi:[1,0] neg_hi:[0,1]
	v_pk_add_f32 v[70:71], v[98:99], v[100:101] op_sel:[0,1] op_sel_hi:[1,0] neg_lo:[0,1]
	v_mov_b32_e32 v98, v0
	s_nop 0
	v_and_b32_e32 v97, -16, v98
	v_and_b32_e32 v99, 15, v98
	v_lshlrev_b32_e32 v100, 3, v97
	v_mad_u32_u24 v100, v99, s5, v100
	v_cmp_ne_u32_e32 vcc, 0, v99
	ds_write2_b64 v100, v[88:89], v[90:91] offset1:1
	ds_write2_b64 v100, v[92:93], v[94:95] offset0:2 offset1:3
	ds_write2_b64 v100, v[80:81], v[82:83] offset0:4 offset1:5
	ds_write2_b64 v100, v[86:87], v[84:85] offset0:6 offset1:7
	ds_write2_b64 v100, v[72:73], v[74:75] offset0:8 offset1:9
	ds_write2_b64 v100, v[76:77], v[78:79] offset0:10 offset1:11
	ds_write2_b64 v100, v[64:65], v[66:67] offset0:12 offset1:13
	ds_write2_b64 v100, v[68:69], v[70:71] offset0:14 offset1:15
	s_waitcnt lgkmcnt(0)
	s_barrier
	s_and_saveexec_b64 s[6:7], vcc
	s_xor_b64 s[6:7], exec, s[6:7]
	v_sub_u32_e32 v99, 16, v99
	v_mul_u32_u24_e32 v99, 0x111, v99
	v_sub_u32_e32 v97, v99, v97
	v_add_u32_e32 v100, 0xf0, v97
	s_andn2_saveexec_b64 s[6:7], s[6:7]
	v_sub_u32_e32 v97, 0x100, v98
	v_cmp_lt_u32_e32 vcc, 15, v98
	s_nop 1
	v_cndmask_b32_e32 v100, 1, v97, vcc
	s_or_b64 exec, exec, s[6:7]
	v_mov_b32_e32 v97, 0
	v_lshlrev_b32_e32 v110, 3, v100
	ds_read_b64 v[108:109], v97
	ds_read2_b64 v[100:103], v110 offset0:14 offset1:15
	v_cmp_eq_u32_e32 vcc, 0, v98
	ds_read2_b64 v[104:107], v110 offset0:12 offset1:13
	s_mov_b32 s6, 0x3f6c835e
	s_mov_b32 s7, 0xbec3ef15
	s_waitcnt lgkmcnt(1)
	v_cndmask_b32_e32 v99, v103, v109, vcc
	v_cndmask_b32_e32 v98, v102, v108, vcc
	v_pk_add_f32 v[102:103], v[88:89], v[98:99] neg_hi:[0,1]
	v_pk_add_f32 v[88:89], v[88:89], v[98:99] neg_lo:[0,1]
	s_mov_b32 s9, s8
	v_pk_mul_f32 v[98:99], v[102:103], v[88:89] op_sel:[0,0] op_sel_hi:[0,1]
	v_pk_fma_f32 v[98:99], v[102:103], v[88:89], v[98:99] op_sel:[1,1,0] op_sel_hi:[1,0,1] neg_hi:[0,1,0]
	v_pk_add_f32 v[88:89], v[90:91], v[100:101] neg_hi:[0,1]
	v_pk_add_f32 v[90:91], v[90:91], v[100:101] neg_lo:[0,1]
	s_mov_b32 s14, s11
	v_pk_add_f32 v[62:63], v[62:63], v[98:99] op_sel:[1,0] op_sel_hi:[0,1] neg_lo:[0,1] neg_hi:[1,1]
	v_pk_mul_f32 v[98:99], v[88:89], v[90:91] op_sel:[0,0] op_sel_hi:[0,1]
	v_pk_fma_f32 v[98:99], v[88:89], v[90:91], v[98:99] op_sel:[1,1,0] op_sel_hi:[1,0,1] neg_hi:[0,1,0]
	s_waitcnt lgkmcnt(0)
	v_pk_add_f32 v[88:89], v[92:93], v[106:107] neg_hi:[0,1]
	v_pk_add_f32 v[90:91], v[92:93], v[106:107] neg_lo:[0,1]
	s_mov_b32 s15, s10
	v_pk_mul_f32 v[92:93], v[88:89], v[90:91] op_sel:[0,0] op_sel_hi:[0,1]
	v_pk_fma_f32 v[92:93], v[88:89], v[90:91], v[92:93] op_sel:[1,1,0] op_sel_hi:[1,0,1] neg_hi:[0,1,0]
	v_pk_add_f32 v[60:61], v[60:61], v[98:99] op_sel:[1,0] op_sel_hi:[0,1] neg_lo:[0,1] neg_hi:[1,1]
	ds_read2_b64 v[88:91], v110 offset0:10 offset1:11
	v_pk_add_f32 v[58:59], v[58:59], v[92:93] op_sel:[1,0] op_sel_hi:[0,1] neg_lo:[0,1] neg_hi:[1,1]
	v_pk_add_f32 v[92:93], v[94:95], v[104:105] neg_hi:[0,1]
	v_pk_add_f32 v[94:95], v[94:95], v[104:105] neg_lo:[0,1]
	s_mov_b32 s13, s12
	v_pk_mul_f32 v[98:99], v[92:93], v[94:95] op_sel:[0,0] op_sel_hi:[0,1]
	v_pk_fma_f32 v[98:99], v[92:93], v[94:95], v[98:99] op_sel:[1,1,0] op_sel_hi:[1,0,1] neg_hi:[0,1,0]
	ds_read2_b64 v[92:95], v110 offset0:8 offset1:9
	v_pk_add_f32 v[56:57], v[56:57], v[98:99] op_sel:[1,0] op_sel_hi:[0,1] neg_lo:[0,1] neg_hi:[1,1]
	s_waitcnt lgkmcnt(1)
	v_pk_add_f32 v[98:99], v[80:81], v[90:91] neg_hi:[0,1]
	v_pk_add_f32 v[80:81], v[80:81], v[90:91] neg_lo:[0,1]
	s_add_u32 s2, s2, 0x2000000
	v_pk_mul_f32 v[90:91], v[98:99], v[80:81] op_sel:[0,0] op_sel_hi:[0,1]
	v_pk_fma_f32 v[90:91], v[98:99], v[80:81], v[90:91] op_sel:[1,1,0] op_sel_hi:[1,0,1] neg_hi:[0,1,0]
	v_pk_add_f32 v[80:81], v[82:83], v[88:89] neg_hi:[0,1]
	v_pk_add_f32 v[82:83], v[82:83], v[88:89] neg_lo:[0,1]
	s_addc_u32 s3, s3, 0
	v_pk_mul_f32 v[88:89], v[80:81], v[82:83] op_sel:[0,0] op_sel_hi:[0,1]
	v_pk_fma_f32 v[88:89], v[80:81], v[82:83], v[88:89] op_sel:[1,1,0] op_sel_hi:[1,0,1] neg_hi:[0,1,0]
	s_waitcnt lgkmcnt(0)
	v_pk_add_f32 v[80:81], v[86:87], v[94:95] neg_lo:[0,1]
	v_pk_add_f32 v[54:55], v[54:55], v[90:91] op_sel:[1,0] op_sel_hi:[0,1] neg_lo:[0,1] neg_hi:[1,1]
	s_load_dwordx2 s[0:1], s[0:1], 0x8
	v_pk_add_f32 v[88:89], v[52:53], v[88:89] op_sel:[1,0] op_sel_hi:[0,1] neg_lo:[0,1] neg_hi:[1,1]
	v_pk_add_f32 v[52:53], v[86:87], v[94:95] neg_hi:[0,1]
	s_nop 0
	v_pk_mul_f32 v[82:83], v[52:53], v[80:81] op_sel:[0,0] op_sel_hi:[0,1]
	v_pk_fma_f32 v[82:83], v[52:53], v[80:81], v[82:83] op_sel:[1,1,0] op_sel_hi:[1,0,1] neg_hi:[0,1,0]
	v_pk_add_f32 v[80:81], v[84:85], v[92:93] neg_hi:[0,1]
	s_nop 0
	v_pk_add_f32 v[86:87], v[50:51], v[82:83] op_sel:[1,0] op_sel_hi:[0,1] neg_lo:[0,1] neg_hi:[1,1]
	ds_read2_b64 v[50:53], v110 offset0:6 offset1:7
	v_pk_add_f32 v[82:83], v[84:85], v[92:93] neg_lo:[0,1]
	s_nop 0
	v_pk_mul_f32 v[84:85], v[80:81], v[82:83] op_sel:[0,0] op_sel_hi:[0,1]
	v_pk_fma_f32 v[84:85], v[80:81], v[82:83], v[84:85] op_sel:[1,1,0] op_sel_hi:[1,0,1] neg_hi:[0,1,0]
	ds_read2_b64 v[80:83], v110 offset0:4 offset1:5
	v_pk_add_f32 v[84:85], v[48:49], v[84:85] op_sel:[1,0] op_sel_hi:[0,1] neg_lo:[0,1] neg_hi:[1,1]
	s_waitcnt lgkmcnt(0)
	v_pk_add_f32 v[48:49], v[72:73], v[52:53] neg_hi:[0,1]
	v_pk_add_f32 v[52:53], v[72:73], v[52:53] neg_lo:[0,1]
	s_nop 0
	v_pk_mul_f32 v[72:73], v[48:49], v[52:53] op_sel:[0,0] op_sel_hi:[0,1]
	v_pk_fma_f32 v[72:73], v[48:49], v[52:53], v[72:73] op_sel:[1,1,0] op_sel_hi:[1,0,1] neg_hi:[0,1,0]
	v_pk_add_f32 v[48:49], v[74:75], v[50:51] neg_lo:[0,1]
	s_nop 0
	v_pk_add_f32 v[52:53], v[46:47], v[72:73] op_sel:[1,0] op_sel_hi:[0,1] neg_lo:[0,1] neg_hi:[1,1]
	v_pk_add_f32 v[46:47], v[74:75], v[50:51] neg_hi:[0,1]
	s_nop 0
	v_pk_mul_f32 v[50:51], v[46:47], v[48:49] op_sel:[0,0] op_sel_hi:[0,1]
	v_pk_fma_f32 v[50:51], v[46:47], v[48:49], v[50:51] op_sel:[1,1,0] op_sel_hi:[1,0,1] neg_hi:[0,1,0]
	v_pk_add_f32 v[46:47], v[76:77], v[82:83] neg_lo:[0,1]
	s_nop 0
	v_pk_add_f32 v[50:51], v[44:45], v[50:51] op_sel:[1,0] op_sel_hi:[0,1] neg_lo:[0,1] neg_hi:[1,1]
	v_pk_add_f32 v[44:45], v[76:77], v[82:83] neg_hi:[0,1]
	s_nop 0
	v_pk_mul_f32 v[48:49], v[44:45], v[46:47] op_sel:[0,0] op_sel_hi:[0,1]
	v_pk_fma_f32 v[48:49], v[44:45], v[46:47], v[48:49] op_sel:[1,1,0] op_sel_hi:[1,0,1] neg_hi:[0,1,0]
	v_pk_add_f32 v[46:47], v[78:79], v[80:81] neg_hi:[0,1]
	s_nop 0
	v_pk_add_f32 v[72:73], v[42:43], v[48:49] op_sel:[1,0] op_sel_hi:[0,1] neg_lo:[0,1] neg_hi:[1,1]
	ds_read2_b64 v[42:45], v110 offset0:2 offset1:3
	v_pk_add_f32 v[48:49], v[78:79], v[80:81] neg_lo:[0,1]
	s_nop 0
	v_pk_mul_f32 v[74:75], v[46:47], v[48:49] op_sel:[0,0] op_sel_hi:[0,1]
	v_pk_fma_f32 v[74:75], v[46:47], v[48:49], v[74:75] op_sel:[1,1,0] op_sel_hi:[1,0,1] neg_hi:[0,1,0]
	ds_read2_b64 v[46:49], v110 offset1:1
	v_pk_add_f32 v[40:41], v[40:41], v[74:75] op_sel:[1,0] op_sel_hi:[0,1] neg_lo:[0,1] neg_hi:[1,1]
	s_waitcnt lgkmcnt(1)
	v_pk_add_f32 v[74:75], v[64:65], v[44:45] neg_hi:[0,1]
	v_pk_add_f32 v[44:45], v[64:65], v[44:45] neg_lo:[0,1]
	s_waitcnt lgkmcnt(0)
	v_pk_mul_f32 v[64:65], v[74:75], v[44:45] op_sel:[0,0] op_sel_hi:[0,1]
	v_pk_fma_f32 v[64:65], v[74:75], v[44:45], v[64:65] op_sel:[1,1,0] op_sel_hi:[1,0,1] neg_hi:[0,1,0]
	v_pk_add_f32 v[44:45], v[66:67], v[42:43] neg_hi:[0,1]
	v_pk_add_f32 v[42:43], v[66:67], v[42:43] neg_lo:[0,1]
	s_barrier
	v_pk_add_f32 v[38:39], v[38:39], v[64:65] op_sel:[1,0] op_sel_hi:[0,1] neg_lo:[0,1] neg_hi:[1,1]
	v_pk_mul_f32 v[64:65], v[44:45], v[42:43] op_sel:[0,0] op_sel_hi:[0,1]
	v_pk_fma_f32 v[64:65], v[44:45], v[42:43], v[64:65] op_sel:[1,1,0] op_sel_hi:[1,0,1] neg_hi:[0,1,0]
	v_pk_add_f32 v[42:43], v[68:69], v[48:49] neg_hi:[0,1]
	v_pk_add_f32 v[44:45], v[68:69], v[48:49] neg_lo:[0,1]
	s_nop 0
	v_pk_mul_f32 v[48:49], v[42:43], v[44:45] op_sel:[0,0] op_sel_hi:[0,1]
	v_pk_fma_f32 v[48:49], v[42:43], v[44:45], v[48:49] op_sel:[1,1,0] op_sel_hi:[1,0,1] neg_hi:[0,1,0]
	v_pk_add_f32 v[42:43], v[70:71], v[46:47] neg_hi:[0,1]
	v_pk_add_f32 v[44:45], v[70:71], v[46:47] neg_lo:[0,1]
	v_pk_add_f32 v[36:37], v[36:37], v[64:65] op_sel:[1,0] op_sel_hi:[0,1] neg_lo:[0,1] neg_hi:[1,1]
	s_nop 0
	v_pk_mul_f32 v[46:47], v[42:43], v[44:45] op_sel:[0,0] op_sel_hi:[0,1]
	v_pk_fma_f32 v[46:47], v[42:43], v[44:45], v[46:47] op_sel:[1,1,0] op_sel_hi:[1,0,1] neg_hi:[0,1,0]
	v_pk_add_f32 v[42:43], v[62:63], v[52:53]
	v_pk_add_f32 v[32:33], v[32:33], v[46:47] op_sel:[1,0] op_sel_hi:[0,1] neg_lo:[0,1] neg_hi:[1,1]
	v_pk_add_f32 v[44:45], v[62:63], v[52:53] neg_lo:[0,1] neg_hi:[0,1]
	v_pk_add_f32 v[46:47], v[54:55], v[38:39]
	v_pk_add_f32 v[38:39], v[54:55], v[38:39] neg_lo:[0,1] neg_hi:[0,1]
	v_pk_add_f32 v[34:35], v[34:35], v[48:49] op_sel:[1,0] op_sel_hi:[0,1] neg_lo:[0,1] neg_hi:[1,1]
	v_pk_add_f32 v[48:49], v[42:43], v[46:47]
	v_pk_add_f32 v[42:43], v[42:43], v[46:47] neg_lo:[0,1] neg_hi:[0,1]
	v_pk_add_f32 v[46:47], v[44:45], v[38:39] op_sel:[0,1] op_sel_hi:[1,0] neg_hi:[0,1]
	v_pk_add_f32 v[38:39], v[44:45], v[38:39] op_sel:[0,1] op_sel_hi:[1,0] neg_lo:[0,1]
	v_pk_add_f32 v[44:45], v[60:61], v[50:51]
	v_pk_add_f32 v[50:51], v[60:61], v[50:51] neg_lo:[0,1] neg_hi:[0,1]
	v_pk_add_f32 v[52:53], v[88:89], v[36:37]
	v_pk_add_f32 v[36:37], v[88:89], v[36:37] neg_lo:[0,1] neg_hi:[0,1]
	v_pk_add_f32 v[54:55], v[44:45], v[52:53]
	v_pk_add_f32 v[44:45], v[44:45], v[52:53] neg_lo:[0,1] neg_hi:[0,1]
	v_pk_add_f32 v[52:53], v[50:51], v[36:37] op_sel:[0,1] op_sel_hi:[1,0] neg_hi:[0,1]
	v_pk_add_f32 v[36:37], v[50:51], v[36:37] op_sel:[0,1] op_sel_hi:[1,0] neg_lo:[0,1]
	v_pk_add_f32 v[50:51], v[58:59], v[72:73]
	v_pk_add_f32 v[58:59], v[58:59], v[72:73] neg_lo:[0,1] neg_hi:[0,1]
	v_pk_add_f32 v[60:61], v[86:87], v[34:35]
	v_pk_add_f32 v[34:35], v[86:87], v[34:35] neg_lo:[0,1] neg_hi:[0,1]
	v_pk_add_f32 v[62:63], v[50:51], v[60:61]
	v_pk_add_f32 v[50:51], v[50:51], v[60:61] neg_lo:[0,1] neg_hi:[0,1]
	v_pk_add_f32 v[60:61], v[58:59], v[34:35] op_sel:[0,1] op_sel_hi:[1,0] neg_hi:[0,1]
	v_pk_add_f32 v[34:35], v[58:59], v[34:35] op_sel:[0,1] op_sel_hi:[1,0] neg_lo:[0,1]
	v_pk_add_f32 v[58:59], v[56:57], v[40:41]
	v_pk_add_f32 v[40:41], v[56:57], v[40:41] neg_lo:[0,1] neg_hi:[0,1]
	v_pk_add_f32 v[56:57], v[84:85], v[32:33]
	v_pk_add_f32 v[32:33], v[84:85], v[32:33] neg_lo:[0,1] neg_hi:[0,1]
	v_pk_add_f32 v[64:65], v[58:59], v[56:57]
	v_pk_add_f32 v[56:57], v[58:59], v[56:57] neg_lo:[0,1] neg_hi:[0,1]
	v_pk_add_f32 v[58:59], v[40:41], v[32:33] op_sel:[0,1] op_sel_hi:[1,0] neg_hi:[0,1]
	v_pk_add_f32 v[32:33], v[40:41], v[32:33] op_sel:[0,1] op_sel_hi:[1,0] neg_lo:[0,1]
	v_pk_mul_f32 v[40:41], v[52:53], s[6:7] op_sel:[0,0] op_sel_hi:[0,1]
	v_pk_fma_f32 v[40:41], v[52:53], s[6:7], v[40:41] op_sel:[1,1,0] op_sel_hi:[1,0,1] neg_lo:[0,1,0]
	v_pk_mul_f32 v[52:53], v[36:37], s[10:11] op_sel:[0,0] op_sel_hi:[0,1]
	v_pk_fma_f32 v[52:53], v[36:37], s[10:11], v[52:53] op_sel:[1,1,0] op_sel_hi:[1,0,1] neg_lo:[0,1,0]
	v_pk_add_f32 v[36:37], v[60:61], v[60:61] op_sel:[0,1] op_sel_hi:[1,0] neg_hi:[0,1]
	v_pk_add_f32 v[44:45], v[44:45], v[44:45] op_sel:[0,1] op_sel_hi:[1,0] neg_hi:[0,1]
	s_nop 0
	v_pk_mul_f32 v[60:61], v[58:59], s[10:11] op_sel:[0,0] op_sel_hi:[0,1]
	v_pk_fma_f32 v[60:61], v[58:59], s[10:11], v[60:61] op_sel:[1,1,0] op_sel_hi:[1,0,1] neg_lo:[0,1,0]
	v_pk_mul_f32 v[58:59], v[32:33], s[14:15] op_sel:[0,0] op_sel_hi:[0,1]
	v_pk_fma_f32 v[58:59], v[32:33], s[14:15], v[58:59] op_sel:[1,1,0] op_sel_hi:[1,0,1] neg_lo:[0,1,0]
	v_pk_add_f32 v[32:33], v[48:49], v[62:63]
	v_pk_mul_f32 v[36:37], v[36:37], s[8:9]
	v_pk_add_f32 v[48:49], v[48:49], v[62:63] neg_lo:[0,1] neg_hi:[0,1]
	v_pk_add_f32 v[62:63], v[54:55], v[64:65]
	v_pk_add_f32 v[54:55], v[54:55], v[64:65] neg_lo:[0,1] neg_hi:[0,1]
	v_pk_mul_f32 v[44:45], v[44:45], s[8:9]
	v_pk_add_f32 v[34:35], v[34:35], v[34:35] op_sel:[0,1] op_sel_hi:[1,0] neg_lo:[0,1]
	v_pk_add_f32 v[56:57], v[56:57], v[56:57] op_sel:[0,1] op_sel_hi:[1,0] neg_lo:[0,1]
	v_pk_add_f32 v[64:65], v[32:33], v[62:63]
	v_pk_add_f32 v[32:33], v[32:33], v[62:63] neg_lo:[0,1] neg_hi:[0,1]
	v_pk_add_f32 v[62:63], v[48:49], v[54:55] op_sel:[0,1] op_sel_hi:[1,0] neg_hi:[0,1]
	v_pk_add_f32 v[48:49], v[48:49], v[54:55] op_sel:[0,1] op_sel_hi:[1,0] neg_lo:[0,1]
	v_pk_add_f32 v[54:55], v[46:47], v[36:37]
	v_pk_add_f32 v[36:37], v[46:47], v[36:37] neg_lo:[0,1] neg_hi:[0,1]
	v_pk_add_f32 v[46:47], v[40:41], v[60:61]
	v_pk_add_f32 v[40:41], v[40:41], v[60:61] neg_lo:[0,1] neg_hi:[0,1]
	v_pk_mul_f32 v[34:35], v[34:35], s[12:13]
	v_pk_mul_f32 v[56:57], v[56:57], s[12:13]
	v_pk_add_f32 v[60:61], v[54:55], v[46:47]
	v_pk_add_f32 v[46:47], v[54:55], v[46:47] neg_lo:[0,1] neg_hi:[0,1]
	v_pk_add_f32 v[54:55], v[36:37], v[40:41] op_sel:[0,1] op_sel_hi:[1,0] neg_hi:[0,1]
	v_pk_add_f32 v[36:37], v[36:37], v[40:41] op_sel:[0,1] op_sel_hi:[1,0] neg_lo:[0,1]
	v_pk_add_f32 v[40:41], v[42:43], v[50:51] op_sel:[0,1] op_sel_hi:[1,0] neg_hi:[0,1]
	v_pk_add_f32 v[42:43], v[42:43], v[50:51] op_sel:[0,1] op_sel_hi:[1,0] neg_lo:[0,1]
	v_pk_add_f32 v[50:51], v[44:45], v[56:57]
	v_pk_add_f32 v[44:45], v[44:45], v[56:57] neg_lo:[0,1] neg_hi:[0,1]
	v_pk_add_f32 v[56:57], v[50:51], v[40:41]
	v_pk_add_f32 v[40:41], v[40:41], v[50:51] neg_lo:[0,1] neg_hi:[0,1]
	v_pk_add_f32 v[50:51], v[42:43], v[44:45] op_sel:[0,1] op_sel_hi:[1,0] neg_hi:[0,1]
	v_pk_add_f32 v[42:43], v[42:43], v[44:45] op_sel:[0,1] op_sel_hi:[1,0] neg_lo:[0,1]
	v_pk_add_f32 v[44:45], v[38:39], v[34:35]
	v_pk_add_f32 v[34:35], v[38:39], v[34:35] neg_lo:[0,1] neg_hi:[0,1]
	v_pk_add_f32 v[38:39], v[52:53], v[58:59]
	v_pk_add_f32 v[52:53], v[52:53], v[58:59] neg_lo:[0,1] neg_hi:[0,1]
	v_pk_add_f32 v[58:59], v[44:45], v[38:39]
	v_pk_add_f32 v[38:39], v[44:45], v[38:39] neg_lo:[0,1] neg_hi:[0,1]
	v_pk_add_f32 v[44:45], v[34:35], v[52:53] op_sel:[0,1] op_sel_hi:[1,0] neg_hi:[0,1]
	v_pk_add_f32 v[34:35], v[34:35], v[52:53] op_sel:[0,1] op_sel_hi:[1,0] neg_lo:[0,1]
	v_pk_mul_f32 v[52:53], v[60:61], v[30:31] op_sel:[0,0] op_sel_hi:[0,1]
	v_pk_fma_f32 v[52:53], v[60:61], v[30:31], v[52:53] op_sel:[1,1,0] op_sel_hi:[1,0,1] neg_lo:[0,1,0]
	v_pk_mul_f32 v[30:31], v[56:57], v[28:29] op_sel:[0,0] op_sel_hi:[0,1]
	v_pk_fma_f32 v[30:31], v[56:57], v[28:29], v[30:31] op_sel:[1,1,0] op_sel_hi:[1,0,1] neg_lo:[0,1,0]
	v_pk_mul_f32 v[28:29], v[58:59], v[26:27] op_sel:[0,0] op_sel_hi:[0,1]
	v_pk_fma_f32 v[28:29], v[58:59], v[26:27], v[28:29] op_sel:[1,1,0] op_sel_hi:[1,0,1] neg_lo:[0,1,0]
	v_pk_mul_f32 v[26:27], v[62:63], v[24:25] op_sel:[0,0] op_sel_hi:[0,1]
	v_pk_fma_f32 v[26:27], v[62:63], v[24:25], v[26:27] op_sel:[1,1,0] op_sel_hi:[1,0,1] neg_lo:[0,1,0]
	v_pk_mul_f32 v[24:25], v[54:55], v[20:21] op_sel:[0,0] op_sel_hi:[0,1]
	v_pk_fma_f32 v[24:25], v[54:55], v[20:21], v[24:25] op_sel:[1,1,0] op_sel_hi:[1,0,1] neg_lo:[0,1,0]
	v_pk_mul_f32 v[20:21], v[50:51], v[16:17] op_sel:[0,0] op_sel_hi:[0,1]
	v_pk_fma_f32 v[20:21], v[50:51], v[16:17], v[20:21] op_sel:[1,1,0] op_sel_hi:[1,0,1] neg_lo:[0,1,0]
	s_nop 0
	v_pk_mul_f32 v[16:17], v[44:45], v[10:11] op_sel:[0,0] op_sel_hi:[0,1]
	v_pk_fma_f32 v[16:17], v[44:45], v[10:11], v[16:17] op_sel:[1,1,0] op_sel_hi:[1,0,1] neg_lo:[0,1,0]
	v_pk_mul_f32 v[10:11], v[32:33], v[22:23] op_sel:[0,0] op_sel_hi:[0,1]
	v_pk_fma_f32 v[10:11], v[32:33], v[22:23], v[10:11] op_sel:[1,1,0] op_sel_hi:[1,0,1] neg_lo:[0,1,0]
	ds_write_b64 v1, v[10:11] offset:17472
	v_pk_mul_f32 v[10:11], v[46:47], v[18:19] op_sel:[0,0] op_sel_hi:[0,1]
	v_pk_fma_f32 v[10:11], v[46:47], v[18:19], v[10:11] op_sel:[1,1,0] op_sel_hi:[1,0,1] neg_lo:[0,1,0]
	ds_write_b64 v1, v[10:11] offset:19656
	v_pk_mul_f32 v[10:11], v[40:41], v[12:13] op_sel:[0,0] op_sel_hi:[0,1]
	v_pk_fma_f32 v[10:11], v[40:41], v[12:13], v[10:11] op_sel:[1,1,0] op_sel_hi:[1,0,1] neg_lo:[0,1,0]
	ds_write_b64 v1, v[10:11] offset:21840
	v_pk_mul_f32 v[10:11], v[38:39], v[14:15] op_sel:[0,0] op_sel_hi:[0,1]
	v_pk_fma_f32 v[10:11], v[38:39], v[14:15], v[10:11] op_sel:[1,1,0] op_sel_hi:[1,0,1] neg_lo:[0,1,0]
	ds_write_b64 v1, v[10:11] offset:24024
	v_pk_mul_f32 v[10:11], v[48:49], v[6:7] op_sel:[0,0] op_sel_hi:[0,1]
	v_pk_fma_f32 v[10:11], v[48:49], v[6:7], v[10:11] op_sel:[1,1,0] op_sel_hi:[1,0,1] neg_lo:[0,1,0]
	v_pk_mul_f32 v[6:7], v[36:37], v[8:9] op_sel:[0,0] op_sel_hi:[0,1]
	v_pk_fma_f32 v[6:7], v[36:37], v[8:9], v[6:7] op_sel:[1,1,0] op_sel_hi:[1,0,1] neg_lo:[0,1,0]
	ds_write_b64 v1, v[6:7] offset:28392
	v_pk_mul_f32 v[6:7], v[42:43], v[4:5] op_sel:[0,0] op_sel_hi:[0,1]
	v_pk_fma_f32 v[6:7], v[42:43], v[4:5], v[6:7] op_sel:[1,1,0] op_sel_hi:[1,0,1] neg_lo:[0,1,0]
	v_pk_mul_f32 v[4:5], v[34:35], v[2:3] op_sel:[0,0] op_sel_hi:[0,1]
	v_pk_fma_f32 v[4:5], v[34:35], v[2:3], v[4:5] op_sel:[1,1,0] op_sel_hi:[1,0,1] neg_lo:[0,1,0]
	ds_write_b64 v1, v[64:65]
	ds_write_b64 v1, v[52:53] offset:2184
	ds_write_b64 v1, v[30:31] offset:4368
	ds_write_b64 v1, v[28:29] offset:6552
	ds_write_b64 v1, v[26:27] offset:8736
	ds_write_b64 v1, v[24:25] offset:10920
	ds_write_b64 v1, v[20:21] offset:13104
	ds_write_b64 v1, v[16:17] offset:15288
	ds_write_b64 v1, v[10:11] offset:26208
	ds_write_b64 v1, v[6:7] offset:30576
	ds_write_b64 v1, v[4:5] offset:32760
	s_waitcnt lgkmcnt(0)
	s_barrier
	ds_read2_b64 v[2:5], v96 offset1:16
	ds_read2_b64 v[6:9], v96 offset0:32 offset1:48
	ds_read2_b64 v[10:13], v96 offset0:64 offset1:80
	ds_read2_b64 v[14:17], v96 offset0:128 offset1:144
	ds_read2_b64 v[18:21], v96 offset0:96 offset1:112
	ds_read2_b64 v[22:25], v96 offset0:192 offset1:208
	ds_read2_b64 v[26:29], v96 offset0:160 offset1:176
	ds_read2_b64 v[30:33], v96 offset0:224 offset1:240
	s_waitcnt lgkmcnt(4)
	v_pk_add_f32 v[34:35], v[2:3], v[14:15]
	v_pk_add_f32 v[2:3], v[2:3], v[14:15] neg_lo:[0,1] neg_hi:[0,1]
	s_waitcnt lgkmcnt(2)
	v_pk_add_f32 v[14:15], v[10:11], v[22:23]
	v_pk_add_f32 v[10:11], v[10:11], v[22:23] neg_lo:[0,1] neg_hi:[0,1]
	v_pk_add_f32 v[22:23], v[34:35], v[14:15]
	v_pk_add_f32 v[14:15], v[34:35], v[14:15] neg_lo:[0,1] neg_hi:[0,1]
	v_pk_add_f32 v[34:35], v[2:3], v[10:11] op_sel:[0,1] op_sel_hi:[1,0] neg_hi:[0,1]
	v_pk_add_f32 v[2:3], v[2:3], v[10:11] op_sel:[0,1] op_sel_hi:[1,0] neg_lo:[0,1]
	v_pk_add_f32 v[10:11], v[4:5], v[16:17]
	v_pk_add_f32 v[4:5], v[4:5], v[16:17] neg_lo:[0,1] neg_hi:[0,1]
	v_pk_add_f32 v[16:17], v[12:13], v[24:25]
	v_pk_add_f32 v[12:13], v[12:13], v[24:25] neg_lo:[0,1] neg_hi:[0,1]
	v_pk_add_f32 v[24:25], v[10:11], v[16:17]
	v_pk_add_f32 v[10:11], v[10:11], v[16:17] neg_lo:[0,1] neg_hi:[0,1]
	v_pk_add_f32 v[16:17], v[4:5], v[12:13] op_sel:[0,1] op_sel_hi:[1,0] neg_hi:[0,1]
	v_pk_add_f32 v[4:5], v[4:5], v[12:13] op_sel:[0,1] op_sel_hi:[1,0] neg_lo:[0,1]
	s_waitcnt lgkmcnt(1)
	v_pk_add_f32 v[12:13], v[6:7], v[26:27]
	v_pk_add_f32 v[6:7], v[6:7], v[26:27] neg_lo:[0,1] neg_hi:[0,1]
	s_waitcnt lgkmcnt(0)
	v_pk_add_f32 v[26:27], v[18:19], v[30:31]
	v_pk_add_f32 v[18:19], v[18:19], v[30:31] neg_lo:[0,1] neg_hi:[0,1]
	v_pk_add_f32 v[30:31], v[12:13], v[26:27]
	v_pk_add_f32 v[12:13], v[12:13], v[26:27] neg_lo:[0,1] neg_hi:[0,1]
	v_pk_add_f32 v[26:27], v[6:7], v[18:19] op_sel:[0,1] op_sel_hi:[1,0] neg_hi:[0,1]
	v_pk_add_f32 v[6:7], v[6:7], v[18:19] op_sel:[0,1] op_sel_hi:[1,0] neg_lo:[0,1]
	v_pk_add_f32 v[18:19], v[8:9], v[28:29]
	v_pk_add_f32 v[8:9], v[8:9], v[28:29] neg_lo:[0,1] neg_hi:[0,1]
	v_pk_add_f32 v[28:29], v[20:21], v[32:33]
	v_pk_add_f32 v[20:21], v[20:21], v[32:33] neg_lo:[0,1] neg_hi:[0,1]
	v_pk_add_f32 v[32:33], v[18:19], v[28:29]
	v_pk_add_f32 v[18:19], v[18:19], v[28:29] neg_lo:[0,1] neg_hi:[0,1]
	v_pk_add_f32 v[28:29], v[8:9], v[20:21] op_sel:[0,1] op_sel_hi:[1,0] neg_hi:[0,1]
	v_pk_add_f32 v[8:9], v[8:9], v[20:21] op_sel:[0,1] op_sel_hi:[1,0] neg_lo:[0,1]
	v_pk_mul_f32 v[20:21], v[16:17], s[6:7] op_sel:[0,0] op_sel_hi:[0,1]
	v_pk_fma_f32 v[20:21], v[16:17], s[6:7], v[20:21] op_sel:[1,1,0] op_sel_hi:[1,0,1] neg_lo:[0,1,0]
	v_pk_mul_f32 v[16:17], v[4:5], s[10:11] op_sel:[0,0] op_sel_hi:[0,1]
	v_pk_fma_f32 v[16:17], v[4:5], s[10:11], v[16:17] op_sel:[1,1,0] op_sel_hi:[1,0,1] neg_lo:[0,1,0]
	v_pk_add_f32 v[4:5], v[26:27], v[26:27] op_sel:[0,1] op_sel_hi:[1,0] neg_hi:[0,1]
	v_pk_add_f32 v[10:11], v[10:11], v[10:11] op_sel:[0,1] op_sel_hi:[1,0] neg_hi:[0,1]
	s_nop 0
	v_pk_mul_f32 v[26:27], v[28:29], s[10:11] op_sel:[0,0] op_sel_hi:[0,1]
	v_pk_fma_f32 v[26:27], v[28:29], s[10:11], v[26:27] op_sel:[1,1,0] op_sel_hi:[1,0,1] neg_lo:[0,1,0]
	v_pk_mul_f32 v[28:29], v[8:9], s[14:15] op_sel:[0,0] op_sel_hi:[0,1]
	v_pk_fma_f32 v[28:29], v[8:9], s[14:15], v[28:29] op_sel:[1,1,0] op_sel_hi:[1,0,1] neg_lo:[0,1,0]
	v_pk_add_f32 v[8:9], v[22:23], v[30:31]
	v_pk_mul_f32 v[4:5], v[4:5], s[8:9]
	v_pk_add_f32 v[22:23], v[22:23], v[30:31] neg_lo:[0,1] neg_hi:[0,1]
	v_pk_add_f32 v[30:31], v[24:25], v[32:33]
	v_pk_add_f32 v[24:25], v[24:25], v[32:33] neg_lo:[0,1] neg_hi:[0,1]
	v_pk_add_f32 v[18:19], v[18:19], v[18:19] op_sel:[0,1] op_sel_hi:[1,0] neg_lo:[0,1]
	v_pk_add_f32 v[32:33], v[8:9], v[30:31]
	v_pk_add_f32 v[30:31], v[8:9], v[30:31] neg_lo:[0,1] neg_hi:[0,1]
	v_pk_add_f32 v[36:37], v[22:23], v[24:25] op_sel:[0,1] op_sel_hi:[1,0] neg_hi:[0,1]
	v_pk_add_f32 v[22:23], v[22:23], v[24:25] op_sel:[0,1] op_sel_hi:[1,0] neg_lo:[0,1]
	v_pk_add_f32 v[8:9], v[34:35], v[4:5]
	v_pk_add_f32 v[4:5], v[34:35], v[4:5] neg_lo:[0,1] neg_hi:[0,1]
	v_pk_add_f32 v[24:25], v[20:21], v[26:27]
	v_pk_add_f32 v[20:21], v[20:21], v[26:27] neg_lo:[0,1] neg_hi:[0,1]
	v_pk_mul_f32 v[10:11], v[10:11], s[8:9]
	v_pk_add_f32 v[6:7], v[6:7], v[6:7] op_sel:[0,1] op_sel_hi:[1,0] neg_lo:[0,1]
	v_pk_mul_f32 v[18:19], v[18:19], s[12:13]
	v_pk_add_f32 v[26:27], v[8:9], v[24:25]
	v_pk_add_f32 v[24:25], v[8:9], v[24:25] neg_lo:[0,1] neg_hi:[0,1]
	v_pk_add_f32 v[34:35], v[4:5], v[20:21] op_sel:[0,1] op_sel_hi:[1,0] neg_hi:[0,1]
	v_pk_add_f32 v[20:21], v[4:5], v[20:21] op_sel:[0,1] op_sel_hi:[1,0] neg_lo:[0,1]
	v_pk_add_f32 v[4:5], v[14:15], v[12:13] op_sel:[0,1] op_sel_hi:[1,0] neg_hi:[0,1]
	v_pk_add_f32 v[8:9], v[14:15], v[12:13] op_sel:[0,1] op_sel_hi:[1,0] neg_lo:[0,1]
	v_pk_add_f32 v[12:13], v[10:11], v[18:19]
	v_pk_mul_f32 v[6:7], v[6:7], s[12:13]
	v_pk_add_f32 v[10:11], v[10:11], v[18:19] neg_lo:[0,1] neg_hi:[0,1]
	v_pk_add_f32 v[14:15], v[12:13], v[4:5]
	v_pk_add_f32 v[12:13], v[4:5], v[12:13] neg_lo:[0,1] neg_hi:[0,1]
	v_pk_add_f32 v[4:5], v[2:3], v[6:7]
	v_pk_add_f32 v[2:3], v[2:3], v[6:7] neg_lo:[0,1] neg_hi:[0,1]
	v_mov_b32_e32 v1, v0
	v_pk_add_f32 v[18:19], v[8:9], v[10:11] op_sel:[0,1] op_sel_hi:[1,0] neg_hi:[0,1]
	v_pk_add_f32 v[10:11], v[8:9], v[10:11] op_sel:[0,1] op_sel_hi:[1,0] neg_lo:[0,1]
	v_pk_add_f32 v[8:9], v[16:17], v[28:29] neg_lo:[0,1] neg_hi:[0,1]
	v_pk_add_f32 v[6:7], v[16:17], v[28:29]
	v_pk_add_f32 v[38:39], v[2:3], v[8:9] op_sel:[0,1] op_sel_hi:[1,0] neg_hi:[0,1]
	v_pk_add_f32 v[40:41], v[2:3], v[8:9] op_sel:[0,1] op_sel_hi:[1,0] neg_lo:[0,1]
	v_ashrrev_i32_e32 v2, 4, v1
	v_lshlrev_b32_e32 v44, 3, v2
	v_add_u32_e32 v45, 0x8800, v44
	v_and_b32_e32 v1, 15, v1
	v_pk_add_f32 v[16:17], v[4:5], v[6:7]
	v_pk_add_f32 v[28:29], v[4:5], v[6:7] neg_lo:[0,1] neg_hi:[0,1]
	ds_read2_b64 v[2:5], v45 offset0:16 offset1:32
	v_mad_u32_u24 v1, v1, s5, v44
	ds_read2_b64 v[6:9], v45 offset0:48 offset1:64
	s_waitcnt lgkmcnt(1)
	v_pk_mul_f32 v[42:43], v[26:27], v[2:3] op_sel:[0,0] op_sel_hi:[0,1]
	v_pk_fma_f32 v[42:43], v[26:27], v[2:3], v[42:43] op_sel:[1,1,0] op_sel_hi:[1,0,1] neg_lo:[0,1,0]
	v_pk_mul_f32 v[26:27], v[14:15], v[4:5] op_sel:[0,0] op_sel_hi:[0,1]
	v_pk_fma_f32 v[26:27], v[14:15], v[4:5], v[26:27] op_sel:[1,1,0] op_sel_hi:[1,0,1] neg_lo:[0,1,0]
	s_waitcnt lgkmcnt(0)
	v_pk_mul_f32 v[14:15], v[16:17], v[6:7] op_sel:[0,0] op_sel_hi:[0,1]
	v_pk_fma_f32 v[14:15], v[16:17], v[6:7], v[14:15] op_sel:[1,1,0] op_sel_hi:[1,0,1] neg_lo:[0,1,0]
	ds_write2_b64 v1, v[26:27], v[14:15] offset0:32 offset1:48
	v_pk_mul_f32 v[14:15], v[36:37], v[8:9] op_sel:[0,0] op_sel_hi:[0,1]
	v_pk_fma_f32 v[14:15], v[36:37], v[8:9], v[14:15] op_sel:[1,1,0] op_sel_hi:[1,0,1] neg_lo:[0,1,0]
	ds_read2_b64 v[2:5], v45 offset0:80 offset1:96
	s_waitcnt lgkmcnt(0)
	v_pk_mul_f32 v[16:17], v[34:35], v[2:3] op_sel:[0,0] op_sel_hi:[0,1]
	v_pk_fma_f32 v[16:17], v[34:35], v[2:3], v[16:17] op_sel:[1,1,0] op_sel_hi:[1,0,1] neg_lo:[0,1,0]
	ds_write2_b64 v1, v[14:15], v[16:17] offset0:64 offset1:80
	v_pk_mul_f32 v[14:15], v[18:19], v[4:5] op_sel:[0,0] op_sel_hi:[0,1]
	v_pk_fma_f32 v[14:15], v[18:19], v[4:5], v[14:15] op_sel:[1,1,0] op_sel_hi:[1,0,1] neg_lo:[0,1,0]
	ds_read2_b64 v[6:9], v45 offset0:112 offset1:128
	ds_read2_b64 v[2:5], v45 offset0:144 offset1:160
	s_waitcnt lgkmcnt(1)
	v_pk_mul_f32 v[16:17], v[38:39], v[6:7] op_sel:[0,0] op_sel_hi:[0,1]
	v_pk_fma_f32 v[16:17], v[38:39], v[6:7], v[16:17] op_sel:[1,1,0] op_sel_hi:[1,0,1] neg_lo:[0,1,0]
	ds_write2_b64 v1, v[14:15], v[16:17] offset0:96 offset1:112
	v_pk_mul_f32 v[14:15], v[30:31], v[8:9] op_sel:[0,0] op_sel_hi:[0,1]
	v_pk_fma_f32 v[14:15], v[30:31], v[8:9], v[14:15] op_sel:[1,1,0] op_sel_hi:[1,0,1] neg_lo:[0,1,0]
	ds_read2_b64 v[6:9], v45 offset0:176 offset1:192
	s_waitcnt lgkmcnt(2)
	v_pk_mul_f32 v[16:17], v[24:25], v[2:3] op_sel:[0,0] op_sel_hi:[0,1]
	v_pk_fma_f32 v[16:17], v[24:25], v[2:3], v[16:17] op_sel:[1,1,0] op_sel_hi:[1,0,1] neg_lo:[0,1,0]
	ds_write2_b64 v1, v[14:15], v[16:17] offset0:128 offset1:144
	v_pk_mul_f32 v[14:15], v[12:13], v[4:5] op_sel:[0,0] op_sel_hi:[0,1]
	v_pk_fma_f32 v[14:15], v[12:13], v[4:5], v[14:15] op_sel:[1,1,0] op_sel_hi:[1,0,1] neg_lo:[0,1,0]
	ds_read2_b64 v[2:5], v45 offset0:208 offset1:224
	s_waitcnt lgkmcnt(2)
	v_pk_mul_f32 v[12:13], v[28:29], v[6:7] op_sel:[0,0] op_sel_hi:[0,1]
	v_pk_fma_f32 v[12:13], v[28:29], v[6:7], v[12:13] op_sel:[1,1,0] op_sel_hi:[1,0,1] neg_lo:[0,1,0]
	ds_write2_b64 v1, v[32:33], v[42:43] offset1:16
	ds_write2_b64 v1, v[14:15], v[12:13] offset0:160 offset1:176
	ds_read_b64 v[6:7], v44 offset:36736
	v_pk_mul_f32 v[12:13], v[22:23], v[8:9] op_sel:[0,0] op_sel_hi:[0,1]
	v_pk_fma_f32 v[12:13], v[22:23], v[8:9], v[12:13] op_sel:[1,1,0] op_sel_hi:[1,0,1] neg_lo:[0,1,0]
	s_waitcnt lgkmcnt(3)
	v_pk_mul_f32 v[8:9], v[20:21], v[2:3] op_sel:[0,0] op_sel_hi:[0,1]
	v_pk_fma_f32 v[8:9], v[20:21], v[2:3], v[8:9] op_sel:[1,1,0] op_sel_hi:[1,0,1] neg_lo:[0,1,0]
	ds_write2_b64 v1, v[12:13], v[8:9] offset0:192 offset1:208
	v_pk_mul_f32 v[2:3], v[10:11], v[4:5] op_sel:[0,0] op_sel_hi:[0,1]
	v_pk_fma_f32 v[2:3], v[10:11], v[4:5], v[2:3] op_sel:[1,1,0] op_sel_hi:[1,0,1] neg_lo:[0,1,0]
	s_waitcnt lgkmcnt(1)
	v_pk_mul_f32 v[4:5], v[40:41], v[6:7] op_sel:[0,0] op_sel_hi:[0,1]
	v_pk_fma_f32 v[4:5], v[40:41], v[6:7], v[4:5] op_sel:[1,1,0] op_sel_hi:[1,0,1] neg_lo:[0,1,0]
	ds_write2_b64 v1, v[2:3], v[4:5] offset0:224 offset1:240
	v_mov_b32_e32 v1, v0
	s_waitcnt lgkmcnt(0)
	s_barrier
	v_mov_b32_e32 v53, 0
	v_and_b32_e32 v2, 15, v1
	v_and_b32_e32 v1, 0x1ffffff0, v1
	v_lshlrev_b32_e32 v1, 3, v1
	v_mad_u32_u24 v1, v2, s5, v1
	ds_read2_b64 v[2:5], v1 offset1:1
	ds_read2_b64 v[6:9], v1 offset0:2 offset1:3
	ds_read2_b64 v[10:13], v1 offset0:8 offset1:9
	ds_read2_b64 v[18:21], v1 offset0:4 offset1:5
	ds_read2_b64 v[22:25], v1 offset0:6 offset1:7
	ds_read2_b64 v[26:29], v1 offset0:12 offset1:13
	ds_read2_b64 v[30:33], v1 offset0:10 offset1:11
	ds_read2_b64 v[34:37], v1 offset0:14 offset1:15
	s_waitcnt lgkmcnt(5)
	v_pk_add_f32 v[14:15], v[2:3], v[10:11]
	v_pk_add_f32 v[2:3], v[2:3], v[10:11] neg_lo:[0,1] neg_hi:[0,1]
	s_waitcnt lgkmcnt(2)
	v_pk_add_f32 v[10:11], v[18:19], v[26:27]
	v_pk_add_f32 v[18:19], v[18:19], v[26:27] neg_lo:[0,1] neg_hi:[0,1]
	v_pk_add_f32 v[26:27], v[14:15], v[10:11]
	v_pk_add_f32 v[16:17], v[14:15], v[10:11] neg_lo:[0,1] neg_hi:[0,1]
	v_pk_add_f32 v[14:15], v[2:3], v[18:19] op_sel:[0,1] op_sel_hi:[1,0] neg_hi:[0,1]
	v_pk_add_f32 v[18:19], v[2:3], v[18:19] op_sel:[0,1] op_sel_hi:[1,0] neg_lo:[0,1]
	v_pk_add_f32 v[2:3], v[4:5], v[12:13]
	v_pk_add_f32 v[10:11], v[20:21], v[28:29]
	v_pk_add_f32 v[4:5], v[4:5], v[12:13] neg_lo:[0,1] neg_hi:[0,1]
	v_pk_add_f32 v[12:13], v[20:21], v[28:29] neg_lo:[0,1] neg_hi:[0,1]
	v_pk_add_f32 v[28:29], v[2:3], v[10:11]
	v_pk_add_f32 v[2:3], v[2:3], v[10:11] neg_lo:[0,1] neg_hi:[0,1]
	v_pk_add_f32 v[10:11], v[4:5], v[12:13] op_sel:[0,1] op_sel_hi:[1,0] neg_hi:[0,1]
	v_pk_add_f32 v[4:5], v[4:5], v[12:13] op_sel:[0,1] op_sel_hi:[1,0] neg_lo:[0,1]
	s_waitcnt lgkmcnt(1)
	v_pk_add_f32 v[12:13], v[6:7], v[30:31]
	s_waitcnt lgkmcnt(0)
	v_pk_add_f32 v[20:21], v[22:23], v[34:35]
	v_pk_add_f32 v[2:3], v[2:3], v[2:3] op_sel:[0,1] op_sel_hi:[1,0] neg_hi:[0,1]
	v_pk_add_f32 v[6:7], v[6:7], v[30:31] neg_lo:[0,1] neg_hi:[0,1]
	v_pk_add_f32 v[22:23], v[22:23], v[34:35] neg_lo:[0,1] neg_hi:[0,1]
	v_pk_add_f32 v[30:31], v[12:13], v[20:21]
	v_pk_add_f32 v[20:21], v[12:13], v[20:21] neg_lo:[0,1] neg_hi:[0,1]
	v_pk_add_f32 v[12:13], v[6:7], v[22:23] op_sel:[0,1] op_sel_hi:[1,0] neg_hi:[0,1]
	v_pk_mul_f32 v[44:45], v[2:3], s[8:9]
	v_pk_add_f32 v[6:7], v[6:7], v[22:23] op_sel:[0,1] op_sel_hi:[1,0] neg_lo:[0,1]
	v_pk_add_f32 v[22:23], v[8:9], v[32:33]
	v_pk_add_f32 v[2:3], v[12:13], v[12:13] op_sel:[0,1] op_sel_hi:[1,0] neg_hi:[0,1]
	v_pk_add_f32 v[8:9], v[8:9], v[32:33] neg_lo:[0,1] neg_hi:[0,1]
	v_pk_add_f32 v[32:33], v[24:25], v[36:37]
	v_pk_mul_f32 v[12:13], v[2:3], s[8:9]
	v_pk_add_f32 v[2:3], v[6:7], v[6:7] op_sel:[0,1] op_sel_hi:[1,0] neg_lo:[0,1]
	v_pk_add_f32 v[24:25], v[24:25], v[36:37] neg_lo:[0,1] neg_hi:[0,1]
	v_pk_add_f32 v[34:35], v[22:23], v[32:33]
	v_pk_add_f32 v[32:33], v[22:23], v[32:33] neg_lo:[0,1] neg_hi:[0,1]
	v_pk_mul_f32 v[54:55], v[2:3], s[12:13]
	v_pk_add_f32 v[36:37], v[8:9], v[24:25] op_sel:[0,1] op_sel_hi:[1,0] neg_hi:[0,1]
	v_pk_add_f32 v[8:9], v[8:9], v[24:25] op_sel:[0,1] op_sel_hi:[1,0] neg_lo:[0,1]
	v_pk_mul_f32 v[22:23], v[4:5], s[10:11] op_sel:[0,0] op_sel_hi:[0,1]
	v_pk_fma_f32 v[22:23], v[4:5], s[10:11], v[22:23] op_sel:[1,1,0] op_sel_hi:[1,0,1] neg_lo:[0,1,0]
	v_pk_add_f32 v[4:5], v[28:29], v[34:35]
	v_pk_add_f32 v[2:3], v[32:33], v[32:33] op_sel:[0,1] op_sel_hi:[1,0] neg_lo:[0,1]
	v_pk_add_f32 v[28:29], v[28:29], v[34:35] neg_lo:[0,1] neg_hi:[0,1]
	v_pk_mul_f32 v[32:33], v[2:3], s[12:13]
	v_pk_add_f32 v[2:3], v[26:27], v[30:31]
	v_pk_add_f32 v[26:27], v[26:27], v[30:31] neg_lo:[0,1] neg_hi:[0,1]
	v_pk_mul_f32 v[24:25], v[10:11], s[6:7] op_sel:[0,0] op_sel_hi:[0,1]
	v_pk_fma_f32 v[24:25], v[10:11], s[6:7], v[24:25] op_sel:[1,1,0] op_sel_hi:[1,0,1] neg_lo:[0,1,0]
	v_pk_mul_f32 v[6:7], v[36:37], s[10:11] op_sel:[0,0] op_sel_hi:[0,1]
	v_pk_fma_f32 v[6:7], v[36:37], s[10:11], v[6:7] op_sel:[1,1,0] op_sel_hi:[1,0,1] neg_lo:[0,1,0]
	v_pk_mul_f32 v[56:57], v[8:9], s[14:15] op_sel:[0,0] op_sel_hi:[0,1]
	v_pk_fma_f32 v[56:57], v[8:9], s[14:15], v[56:57] op_sel:[1,1,0] op_sel_hi:[1,0,1] neg_lo:[0,1,0]
	v_pk_add_f32 v[10:11], v[2:3], v[4:5]
	v_lshlrev_b32_e32 v34, 2, v0
	v_pk_add_f32 v[4:5], v[2:3], v[4:5] neg_lo:[0,1] neg_hi:[0,1]
	v_pk_add_f32 v[8:9], v[26:27], v[28:29] op_sel:[0,1] op_sel_hi:[1,0] neg_hi:[0,1]
	v_pk_add_f32 v[2:3], v[26:27], v[28:29] op_sel:[0,1] op_sel_hi:[1,0] neg_lo:[0,1]
	v_pk_add_f32 v[26:27], v[14:15], v[12:13]
	v_pk_add_f32 v[28:29], v[24:25], v[6:7]
	v_add_u32_e32 v1, 0x400, v34
	v_pk_add_f32 v[14:15], v[14:15], v[12:13] neg_lo:[0,1] neg_hi:[0,1]
	v_pk_add_f32 v[30:31], v[24:25], v[6:7] neg_lo:[0,1] neg_hi:[0,1]
	v_pk_add_f32 v[12:13], v[26:27], v[28:29]
	v_pk_add_f32 v[6:7], v[26:27], v[28:29] neg_lo:[0,1] neg_hi:[0,1]
	v_add_u32_e32 v24, 0x800, v34
	v_add_u32_e32 v25, 0xc00, v34
	v_add_u32_e32 v26, 0x1000, v34
	v_add_u32_e32 v27, 0x1400, v34
	v_add_u32_e32 v28, 0x1800, v34
	v_add_u32_e32 v29, 0x1c00, v34
	v_add_u32_e32 v35, 0x2000, v34
	s_waitcnt vmcnt(0)
	v_mov_b32_e32 v1, v113
	s_nop 0
	v_mov_b32_e32 v36, v114
	v_mov_b32_e32 v37, v115
	v_mov_b32_e32 v38, v116
	v_mov_b32_e32 v39, v117
	v_mov_b32_e32 v40, v118
	v_mov_b32_e32 v41, v119
	v_mov_b32_e32 v42, v120
	v_add_u32_e32 v24, 0x2400, v34
	v_add_u32_e32 v25, 0x2800, v34
	v_add_u32_e32 v26, 0x2c00, v34
	v_add_u32_e32 v27, 0x3000, v34
	v_add_u32_e32 v28, 0x3400, v34
	v_add_u32_e32 v35, 0x3800, v34
	v_mov_b32_e32 v52, v112
	v_mov_b32_e32 v43, v126
	v_add_u32_e32 v29, 0x3c00, v34
	v_mov_b32_e32 v47, v121
	v_mov_b32_e32 v48, v122
	v_mov_b32_e32 v49, v123
	v_mov_b32_e32 v50, v124
	v_mov_b32_e32 v51, v125
	v_mov_b32_e32 v46, v127
	v_pk_add_f32 v[26:27], v[16:17], v[20:21] op_sel:[0,1] op_sel_hi:[1,0] neg_hi:[0,1]
	v_pk_add_f32 v[16:17], v[16:17], v[20:21] op_sel:[0,1] op_sel_hi:[1,0] neg_lo:[0,1]
	v_pk_add_f32 v[20:21], v[44:45], v[32:33]
	v_pk_add_f32 v[28:29], v[44:45], v[32:33] neg_lo:[0,1] neg_hi:[0,1]
	v_pk_add_f32 v[24:25], v[14:15], v[30:31] op_sel:[0,1] op_sel_hi:[1,0] neg_hi:[0,1]
	v_pk_add_f32 v[14:15], v[14:15], v[30:31] op_sel:[0,1] op_sel_hi:[1,0] neg_lo:[0,1]
	v_pk_add_f32 v[30:31], v[20:21], v[26:27]
	v_pk_add_f32 v[20:21], v[26:27], v[20:21] neg_lo:[0,1] neg_hi:[0,1]
	v_pk_add_f32 v[26:27], v[16:17], v[28:29] op_sel:[0,1] op_sel_hi:[1,0] neg_hi:[0,1]
	v_pk_add_f32 v[16:17], v[16:17], v[28:29] op_sel:[0,1] op_sel_hi:[1,0] neg_lo:[0,1]
	v_pk_add_f32 v[28:29], v[18:19], v[54:55]
	v_pk_add_f32 v[44:45], v[22:23], v[56:57]
	s_mov_b32 s2, 0xff61b1e6
	v_pk_add_f32 v[18:19], v[18:19], v[54:55] neg_lo:[0,1] neg_hi:[0,1]
	v_pk_add_f32 v[54:55], v[22:23], v[56:57] neg_lo:[0,1] neg_hi:[0,1]
	v_pk_add_f32 v[32:33], v[28:29], v[44:45]
	v_pk_add_f32 v[22:23], v[28:29], v[44:45] neg_lo:[0,1] neg_hi:[0,1]
	v_max3_f32 v44, v10, s2, v12
	v_max3_f32 v44, v44, v30, v32
	v_max3_f32 v44, v44, v8, v24
	v_pk_add_f32 v[28:29], v[18:19], v[54:55] op_sel:[0,1] op_sel_hi:[1,0] neg_hi:[0,1]
	v_pk_add_f32 v[18:19], v[18:19], v[54:55] op_sel:[0,1] op_sel_hi:[1,0] neg_lo:[0,1]
	v_max3_f32 v45, -v11, s2, -v13
	v_max3_f32 v44, v44, v26, v28
	v_max3_f32 v44, v44, v4, v6
	v_max3_f32 v44, v44, v20, v22
	v_max3_f32 v44, v44, v2, v14
	v_max3_f32 v44, v44, v16, v18
	v_max3_f32 v45, v45, -v31, -v33
	v_max3_f32 v45, v45, -v9, -v25
	v_mov_b32_dpp v53, v44 quad_perm:[1,0,3,2] row_mask:0xf bank_mask:0xf
	v_max_f32_e32 v53, v53, v53
	v_max_f32_e32 v44, v44, v53
	v_mov_b32_e32 v53, 0
	v_max3_f32 v45, v45, -v27, -v29
	v_max3_f32 v45, v45, -v5, -v7
	v_mov_b32_dpp v53, v44 quad_perm:[2,3,0,1] row_mask:0xf bank_mask:0xf
	v_max_f32_e32 v53, v53, v53
	v_max_f32_e32 v44, v44, v53
	v_mov_b32_e32 v53, 0
	v_max3_f32 v45, v45, -v21, -v23
	v_max3_f32 v45, v45, -v3, -v15
	v_mov_b32_dpp v53, v44 row_half_mirror row_mask:0xf bank_mask:0xf
	v_max_f32_e32 v53, v53, v53
	v_max_f32_e32 v44, v44, v53
	v_mov_b32_e32 v53, 0
	v_max3_f32 v45, v45, -v17, -v19
	s_nop 0
	v_mov_b32_dpp v53, v44 row_mirror row_mask:0xf bank_mask:0xf
	v_max_f32_e32 v53, v53, v53
	v_max_f32_e32 v44, v44, v53
	s_nop 0
	v_readlane_b32 s5, v44, 0
	v_readlane_b32 s6, v44, 16
	v_readlane_b32 s7, v44, 32
	v_readlane_b32 s8, v44, 48
	v_mov_b32_e32 v44, 0
	s_nop 1
	v_mov_b32_dpp v44, v45 quad_perm:[1,0,3,2] row_mask:0xf bank_mask:0xf
	v_max_f32_e32 v44, v44, v44
	v_max_f32_e32 v44, v45, v44
	v_mov_b32_e32 v45, 0
	s_nop 1
	v_mov_b32_dpp v45, v44 quad_perm:[2,3,0,1] row_mask:0xf bank_mask:0xf
	v_max_f32_e32 v45, v45, v45
	v_max_f32_e32 v44, v44, v45
	v_mov_b32_e32 v45, 0
	s_nop 1
	v_mov_b32_dpp v45, v44 row_half_mirror row_mask:0xf bank_mask:0xf
	v_max_f32_e32 v45, v45, v45
	v_max_f32_e32 v44, v44, v45
	v_mov_b32_e32 v45, 0
	s_nop 1
	v_mov_b32_dpp v45, v44 row_mirror row_mask:0xf bank_mask:0xf
	v_max_f32_e32 v45, v45, v45
	v_max_f32_e32 v44, v44, v45
	v_and_b32_e32 v45, 63, v0
	v_readlane_b32 s9, v44, 0
	v_readlane_b32 s10, v44, 16
	v_readlane_b32 s11, v44, 32
	v_readlane_b32 s12, v44, 48
	v_ashrrev_i32_e32 v44, 6, v0
	v_cmp_eq_u32_e32 vcc, 0, v45
	v_lshlrev_b32_e32 v61, 3, v44
	s_and_saveexec_b64 s[2:3], vcc
	s_cbranch_execz .LBB1_10
	v_max_f32_e64 v44, s12, s12
	v_max_f32_e64 v45, s11, s11
	v_max_f32_e32 v44, v45, v44
	v_mov_b32_e32 v45, s10
	v_max3_f32 v45, s9, v45, v44
	v_max_f32_e64 v44, s8, s8
	v_max_f32_e64 v53, s7, s7
	v_max_f32_e32 v44, v53, v44
	v_mov_b32_e32 v53, s6
	v_max3_f32 v44, s5, v53, v44
	ds_write_b64 v61, v[44:45] offset:36864
